# attention K tile in LDS padded by 128 B after rows 15 and 47 so K-fragment ds_read_b128 are bank-conflict free (K buffer 1 and the gains scratch moved up)
# speedup vs baseline: 1.0042x; 1.0004x over previous
.LBB0_512:
	s_add_i32 s0, s79, 0x26b00
	v_mov_b32_e32 v1, s0
	s_add_i32 s0, s79, 0x26b04
	v_mov_b32_e32 v2, s0
	ds_read_b32 v1, v1
	ds_read_b32 v2, v2
	s_cmp_lg_u32 s2, 0
	s_waitcnt lgkmcnt(0)
	v_readfirstlane_b32 s4, v1
	v_readfirstlane_b32 s3, v2
	s_cbranch_scc0 .LBB0_542
	s_lshl_b32 s16, s2, 1
	s_add_u32 s11, s72, 0x11a00000
	s_mov_b64 s[0:1], src_shared_base
	s_addc_u32 s12, s73, 0
	s_add_u32 s0, s72, 0x700000
	v_writelane_b32 v255, s0, 17
	s_addc_u32 s0, s73, 0
	v_writelane_b32 v255, s0, 18
	s_add_u32 s0, s72, 0x780000
	v_writelane_b32 v255, s0, 19
	s_addc_u32 s0, s73, 0
	v_writelane_b32 v255, s0, 20
	s_add_u32 s0, s72, 0x880000
	v_writelane_b32 v255, s0, 21
	s_addc_u32 s0, s73, 0
	v_writelane_b32 v255, s0, 22
	s_mov_b32 s5, s71
	v_readlane_b32 s6, v255, 6
	s_lshl_b32 s70, s6, 10
	v_readlane_b32 s7, v255, 7
	s_add_u32 s80, s72, 0x2da00000
	s_addc_u32 s85, s73, 0
	v_writelane_b32 v255, s4, 23
	s_lshl_b64 s[6:7], s[70:71], 2
	s_add_u32 s0, s4, s6
	v_writelane_b32 v255, s5, 24
	s_addc_u32 s7, s3, s7
	v_readlane_b32 s3, v255, 16
	s_lshl_b32 s2, s3, 7
	s_and_b32 s4, s2, 0xfffff000
	s_lshl_b32 s2, s3, 8
	s_and_b32 s2, s2, 0x700
	s_or_b32 s2, s2, s4
	s_xor_b32 s2, s2, 0xf00
	s_bfe_u32 s6, s3, 0x20003
	s_ashr_i32 s3, s2, 31
	s_lshl_b64 s[2:3], s[2:3], 11
	s_add_u32 s2, s11, s2
	s_addc_u32 s3, s12, s3
	s_lshl_b32 s8, s6, 8
	s_add_u32 s9, s2, s8
	s_addc_u32 s10, s3, 0
	s_ashr_i32 s5, s4, 31
	s_lshl_b64 s[2:3], s[4:5], 11
	s_add_u32 s2, s11, s2
	s_addc_u32 s3, s12, s3
	s_add_u32 s2, s2, s8
	s_addc_u32 s3, s3, 0
	s_add_u32 s2, s2, 0x400
	s_addc_u32 s3, s3, 0
	s_mul_hi_i32 s5, s4, 0x6800
	s_mulk_i32 s4, 0x6800
	s_add_u32 s4, s80, s4
	s_addc_u32 s5, s85, s5
	s_lshl_b32 s8, s6, 9
	s_add_u32 s4, s4, s8
	s_addc_u32 s5, s5, 0
	s_add_u32 s4, s4, 0x800
	s_addc_u32 s5, s5, 0
	s_lshl_b32 s6, s6, 10
	s_add_u32 s6, s0, s6
	v_and_b32_e32 v1, 63, v0
	s_addc_u32 s7, s7, 0
	v_lshlrev_b32_e32 v160, 4, v1
	s_waitcnt vmcnt(0) lgkmcnt(0)
	s_barrier
	v_lshl_add_u64 v[2:3], s[6:7], 0, v[160:161]
	flat_load_dwordx4 v[2:5], v[2:3]
	v_add_u32_e32 v165, s67, v0
	v_writelane_b32 v255, s11, 25
	v_readfirstlane_b32 s0, v165
	v_lshrrev_b32_e32 v8, 1, v0
	s_ashr_i32 s0, s0, 6
	v_writelane_b32 v255, s12, 26
	v_and_b32_e32 v6, 31, v0
	v_bfe_u32 v12, v0, 4, 2
	v_bfe_u32 v14, v0, 2, 3
	v_lshlrev_b32_e32 v10, 3, v0
	v_and_b32_e32 v16, 16, v8
	s_add_i32 s6, s79, 0x18300
	s_lshl_b32 s7, s0, 3
	s_lshl_b32 s8, s0, 2
	v_and_b32_e32 v13, 15, v0
	v_and_b32_e32 v15, 32, v0
	v_bitop3_b32 v0, v12, v0, 15 bitop3:0x78
	v_and_b32_e32 v8, 8, v8
	v_and_b32_e32 v17, 24, v10
	v_lshl_or_b32 v10, v6, 11, v16
	s_lshl_b32 s11, s0, 11
	s_lshl_b32 s12, s0, 12
	v_writelane_b32 v255, s6, 27
	v_add_u32_e32 v18, s6, v160
	s_lshl_b32 s6, s0, 5
	v_or_b32_e32 v6, s7, v12
	v_bitop3_b32 v12, s7, v228, v14 bitop3:0xc8
	s_and_b32 s0, s8, 4
	v_lshlrev_b32_e32 v0, 4, v0
	v_or3_b32 v8, v8, v12, s0
	v_lshl_or_b32 v0, v6, 11, v0
	v_or_b32_e32 v6, 4, v6
	v_mul_u32_u24_e32 v8, 0x3400, v8
	v_bitop3_b32 v12, v6, v13, 7 bitop3:0x6c
	v_lshlrev_b32_e32 v6, 11, v6
	v_or3_b32 v8, v15, v17, v8
	v_mov_b32_e32 v1, v161
	v_mov_b32_e32 v7, v161
	v_mov_b32_e32 v9, v161
	v_lshl_or_b32 v6, v12, 4, v6
	v_lshlrev_b32_e32 v8, 1, v8
	s_add_i32 s13, s79, 0x10000
	v_lshl_add_u64 v[0:1], s[2:3], 0, v[0:1]
	v_lshl_add_u64 v[6:7], s[2:3], 0, v[6:7]
	v_lshl_add_u64 v[8:9], s[4:5], 0, v[8:9]
	s_mov_b64 s[2:3], 0x180
	s_add_i32 s8, s11, s13
	s_add_i32 s98, s11, 0x1000
	s_lshr_b32 s98, s98, 13
	s_lshl_b32 s98, s98, 7
	s_add_i32 s8, s8, s98
	v_lshl_add_u64 v[16:17], v[8:9], 0, s[2:3]
	s_add_i32 s11, s12, s79
	s_ashr_i32 s7, s6, 31
	s_add_i32 s0, s8, 0x400
	v_writelane_b32 v255, s13, 28
	s_add_i32 s12, s11, 0x400
	s_add_i32 s13, s11, 0x800
	s_add_i32 s14, s11, 0xc00
	s_lshl_b64 s[6:7], s[6:7], 11
	s_add_u32 s6, s9, s6
	v_lshl_add_u64 v[12:13], v[8:9], 0, s[86:87]
	v_mov_b32_e32 v11, v161
	s_addc_u32 s7, s10, s7
	v_lshl_add_u64 v[14:15], v[8:9], 0, s[62:63]
	v_lshl_add_u64 v[10:11], s[6:7], 0, v[10:11]
	v_cmp_eq_u32_e64 s[4:5], 0, v165
	s_add_i32 s3, s79, 0x18820
	s_add_i32 s89, s79, 0x18200
	v_writelane_b32 v255, s4, 29
	s_add_i32 s70, s79, 0x18810
	s_mov_b32 s71, s1
	v_writelane_b32 v255, s5, 30
	s_add_i32 s4, s79, 0x18800
	s_mov_b32 s5, s1
	v_writelane_b32 v255, s4, 31
	s_add_i32 s74, s79, 0x1880c
	s_mov_b32 s75, s1
	v_writelane_b32 v255, s5, 32
	v_writelane_b32 v255, s3, 33
	s_add_i32 s3, s79, 0x14100
	v_writelane_b32 v255, s3, 34
	s_add_i32 s4, s79, 0x18804
	s_waitcnt vmcnt(0) lgkmcnt(0)
	ds_write_b128 v18, v[2:5]
	s_mov_b32 s2, m0
	s_mov_b32 m0, s8
	s_nop 0
	global_load_lds_dwordx4 v[0:1], off
	s_mov_b32 m0, s2
	s_mov_b32 s5, s1
	s_mov_b32 s2, m0
	s_mov_b32 m0, s0
	s_nop 0
	global_load_lds_dwordx4 v[6:7], off
	s_mov_b32 m0, s2
	s_mov_b32 s0, m0
	s_mov_b32 m0, s11
	s_nop 0
	global_load_lds_dwordx4 v[8:9], off
	s_mov_b32 m0, s0
	v_writelane_b32 v255, s4, 35
	s_mov_b32 s0, m0
	s_mov_b32 m0, s12
	s_nop 0
	global_load_lds_dwordx4 v[12:13], off
	s_mov_b32 m0, s0
	s_max_u32 s3, s16, 1
	s_mov_b32 s0, m0
	s_mov_b32 m0, s13
	s_nop 0
	global_load_lds_dwordx4 v[14:15], off
	s_mov_b32 m0, s0
	s_mov_b32 s2, 0
	s_mov_b32 s0, m0
	s_mov_b32 m0, s14
	s_nop 0
	global_load_lds_dwordx4 v[16:17], off
	s_mov_b32 m0, s0
	flat_load_dwordx4 v[128:131], v[10:11]
	flat_load_dwordx4 v[132:135], v[10:11] offset:32
	flat_load_dwordx4 v[136:139], v[10:11] offset:64
	flat_load_dwordx4 v[140:143], v[10:11] offset:96
	flat_load_dwordx4 v[144:147], v[10:11] offset:128
	flat_load_dwordx4 v[148:151], v[10:11] offset:160
	flat_load_dwordx4 v[152:155], v[10:11] offset:192
	flat_load_dwordx4 v[166:169], v[10:11] offset:224
	v_writelane_b32 v255, s5, 36
	v_writelane_b32 v255, s16, 37
	v_writelane_b32 v255, s3, 38
	s_add_i32 s3, s79, 0x18204
	v_writelane_b32 v255, s3, 39
	v_writelane_b32 v255, s15, 40
	v_writelane_b32 v255, s79, 41
	v_writelane_b32 v255, s80, 43
	v_writelane_b32 v255, s85, 44
	s_add_i32 s0, s79, 0x18808
	s_add_i32 s76, s79, 0x18814
	s_mov_b32 s77, s1
	v_writelane_b32 v255, s89, 45
	s_branch .LBB0_515

.LBB0_517:
	s_or_b64 exec, exec, s[4:5]
	s_lshr_b32 s3, s2, 1
	s_mul_i32 s3, s15, s3
	v_readlane_b32 s4, v255, 16
	s_add_i32 s33, s4, s3
	s_lshl_b32 s3, s33, 7
	s_and_b32 s6, s3, 0xfffff000
	s_lshl_b32 s3, s33, 8
	s_ashr_i32 s82, s33, 3
	s_and_b32 s3, s3, 0x700
	s_and_b32 s2, s2, 1
	s_and_b32 s69, s82, 3
	s_xor_b32 s4, s3, 0xf00
	s_cmp_eq_u32 s2, 0
	s_mov_b32 s2, s6
	s_cselect_b32 s84, s4, s3
	v_writelane_b32 v255, s2, 46
	s_ashr_i32 s7, s6, 31
	s_lshl_b64 s[66:67], s[6:7], 11
	v_writelane_b32 v255, s3, 47
	v_mov_b32_e32 v0, v165
	v_readlane_b32 s2, v255, 25
	s_add_u32 s2, s2, s66
	v_readlane_b32 s3, v255, 26
	s_addc_u32 s3, s3, s67
	s_lshl_b32 s4, s69, 8
	s_add_u32 s6, s2, s4
	s_addc_u32 s7, s3, 0
	s_add_u32 s3, s6, 0x400
	v_writelane_b32 v255, s4, 48
	s_addc_u32 s68, s7, 0
	s_ashr_i32 s83, s82, 31
	s_lshl_b64 s[4:5], s[82:83], 14
	v_readlane_b32 s2, v255, 17
	s_add_u32 s8, s2, s4
	v_readlane_b32 s2, v255, 18
	s_addc_u32 s9, s2, s5
	s_lshl_b32 s4, s82, 6
	s_ashr_i32 s5, s4, 31
	s_lshl_b64 s[4:5], s[4:5], 2
	v_readlane_b32 s2, v255, 21
	s_add_u32 s4, s2, s4
	v_readlane_b32 s2, v255, 22
	s_addc_u32 s5, s2, s5
	v_mov_b32_e32 v3, v161
	v_readfirstlane_b32 s2, v0
	s_ashr_i32 s10, s2, 6
	s_lshl_b32 s12, s10, 5
	s_mov_b32 s2, s12
	v_and_b32_e32 v39, 63, v0
	v_writelane_b32 v255, s2, 49
	s_add_i32 s94, s12, s84
	v_lshlrev_b32_e32 v2, 2, v39
	v_writelane_b32 v255, s3, 50
	s_lshl_b32 s2, s10, 11
	v_lshl_add_u64 v[4:5], s[4:5], 0, v[2:3]
	v_readlane_b32 s11, v255, 28
	s_lshl_b32 s4, s10, 12
	s_ashr_i32 s95, s94, 31
	s_lshl_b32 s78, s10, 3
	flat_load_dword v3, v[4:5]
	s_add_i32 s2, s2, s11
	s_add_i32 s98, s10, 2
	s_lshr_b32 s98, s98, 2
	s_lshl_b32 s98, s98, 7
	s_add_i32 s2, s2, s98
	s_add_i32 s81, s4, s79
	s_lshl_b64 s[12:13], s[94:95], 2
	v_and_b32_e32 v175, 31, v0
	s_add_u32 s4, s8, s12
	v_writelane_b32 v255, s12, 51
	s_addc_u32 s5, s9, s13
	v_lshlrev_b32_e32 v160, 2, v175
	v_lshl_add_u64 v[4:5], s[4:5], 0, v[160:161]
	flat_load_dword v178, v[4:5]
	v_bfe_u32 v4, v0, 4, 2
	v_bitop3_b32 v6, v4, v0, 15 bitop3:0x78
	v_add_u32_e32 v2, s89, v2
	v_writelane_b32 v255, s13, 52
	v_bfe_u32 v176, v0, 5, 1
	v_lshlrev_b32_e32 v6, 4, v6
	v_or_b32_e32 v4, s78, v4
	v_and_b32_e32 v5, 15, v0
	v_lshlrev_b32_e32 v1, 2, v176
	s_mulk_i32 s10, 0x1c00
	v_lshl_or_b32 v170, v4, 11, v6
	v_or_b32_e32 v4, 4, v4
	v_readlane_b32 s4, v255, 33
	v_lshlrev_b32_e32 v40, 4, v39
	v_sub_u32_e32 v7, v175, v1
	v_bitop3_b32 v5, v4, v5, 7 bitop3:0x6c
	v_lshlrev_b32_e32 v4, 11, v4
	s_add_i32 s4, s4, s10
	v_add_u32_e32 v180, s94, v7
	v_lshl_or_b32 v172, v5, 4, v4
	v_add_u32_e32 v181, s4, v40
	v_lshlrev_b32_e32 v174, 4, v176
	s_waitcnt vmcnt(0) lgkmcnt(0)
	ds_write_b32 v2, v3
	s_waitcnt vmcnt(0)
	ds_write_b128 v181, v[128:131]
	ds_write_b128 v181, v[132:135] offset:1024
	ds_write_b128 v181, v[136:139] offset:2048
	ds_write_b128 v181, v[140:143] offset:3072
	ds_write_b128 v181, v[144:147] offset:4096
	ds_write_b128 v181, v[148:151] offset:5120
	ds_write_b128 v181, v[152:155] offset:6144
	s_add_u32 s4, s6, 0x20400
	s_addc_u32 s5, s7, 0
	v_mov_b32_e32 v171, v161
	v_lshl_add_u64 v[2:3], s[4:5], 0, v[170:171]
	s_add_i32 s96, s2, 0x4100
	s_mov_b32 s6, m0
	s_mov_b32 m0, s96
	s_nop 0
	global_load_lds_dwordx4 v[2:3], off
	s_mov_b32 m0, s6
	v_mov_b32_e32 v173, v161
	v_lshl_add_u64 v[2:3], s[4:5], 0, v[172:173]
	s_add_i32 s97, s2, 0x4500
	s_mov_b32 s4, m0
	s_mov_b32 m0, s97
	s_nop 0
	global_load_lds_dwordx4 v[2:3], off
	s_mov_b32 m0, s4
	s_waitcnt lgkmcnt(0)
	s_barrier
	v_lshlrev_b32_e32 v2, 4, v0
	s_movk_i32 s4, 0x70
	v_and_b32_e32 v34, 16, v175
	v_lshlrev_b32_e32 v34, 3, v34
	v_lshl_add_u32 v34, v175, 8, v34
	v_and_b32_e32 v3, 0x70, v2
	v_bitop3_b32 v35, v174, v2, s4 bitop3:0x78
	s_movk_i32 s4, 0x60
	v_add_u32_e32 v4, s11, v34
	v_bitop3_b32 v36, v174, v3, 32 bitop3:0x36
	v_bitop3_b32 v37, v174, v3, 64 bitop3:0x36
	v_bitop3_b32 v38, v174, v3, s4 bitop3:0x36
	v_add_u32_e32 v182, v35, v4
	v_add_u32_e32 v183, v36, v4
	v_add_u32_e32 v184, v37, v4
	v_add_u32_e32 v185, v38, v4
	ds_read_b128 v[2:5], v182 offset:0
	ds_read_b128 v[6:9], v182 offset:0x2080
	ds_read_b128 v[10:13], v181 offset:0
	ds_read_b128 v[42:45], v183 offset:0
	ds_read_b128 v[46:49], v183 offset:0x2080
	ds_read_b128 v[50:53], v181 offset:0x400
	s_waitcnt lgkmcnt(3)
	s_nop 0
	v_mfma_f32_32x32x16_bf16 v[18:33], v[2:5], v[10:13], 0
	v_mfma_f32_32x32x16_bf16 v[2:17], v[6:9], v[10:13], 0
	ds_read_b128 v[54:57], v184 offset:0
	ds_read_b128 v[58:61], v184 offset:0x2080
	ds_read_b128 v[62:65], v181 offset:0x800
	s_waitcnt lgkmcnt(3)
	v_mfma_f32_32x32x16_bf16 v[18:33], v[42:45], v[50:53], v[18:33]
	v_mfma_f32_32x32x16_bf16 v[2:17], v[46:49], v[50:53], v[2:17]
	ds_read_b128 v[42:45], v185 offset:0
	ds_read_b128 v[46:49], v185 offset:0x2080
	ds_read_b128 v[50:53], v181 offset:0xc00
	s_waitcnt lgkmcnt(3)
	v_mfma_f32_32x32x16_bf16 v[18:33], v[54:57], v[62:65], v[18:33]
	v_mfma_f32_32x32x16_bf16 v[2:17], v[58:61], v[62:65], v[2:17]
	ds_read_b128 v[54:57], v182 offset:0x80
	ds_read_b128 v[58:61], v182 offset:0x2100
	ds_read_b128 v[62:65], v181 offset:0x1000
	s_waitcnt lgkmcnt(3)
	v_mfma_f32_32x32x16_bf16 v[18:33], v[42:45], v[50:53], v[18:33]
	v_mfma_f32_32x32x16_bf16 v[2:17], v[46:49], v[50:53], v[2:17]
	ds_read_b128 v[42:45], v183 offset:0x80
	ds_read_b128 v[46:49], v183 offset:0x2100
	ds_read_b128 v[50:53], v181 offset:0x1400
	s_waitcnt lgkmcnt(3)
	v_mfma_f32_32x32x16_bf16 v[18:33], v[54:57], v[62:65], v[18:33]
	v_mfma_f32_32x32x16_bf16 v[2:17], v[58:61], v[62:65], v[2:17]
	ds_read_b128 v[54:57], v184 offset:0x80
	ds_read_b128 v[58:61], v184 offset:0x2100
	ds_read_b128 v[62:65], v181 offset:0x1800
	s_waitcnt lgkmcnt(3)
	v_mfma_f32_32x32x16_bf16 v[18:33], v[42:45], v[50:53], v[18:33]
	v_mfma_f32_32x32x16_bf16 v[2:17], v[46:49], v[50:53], v[2:17]
	ds_read_b128 v[42:45], v185 offset:0x80
	ds_read_b128 v[46:49], v185 offset:0x2100
	s_waitcnt lgkmcnt(2)
	v_mfma_f32_32x32x16_bf16 v[18:33], v[54:57], v[62:65], v[18:33]
	v_mfma_f32_32x32x16_bf16 v[2:17], v[58:61], v[62:65], v[2:17]
	s_waitcnt lgkmcnt(0)
	v_mfma_f32_32x32x16_bf16 v[18:33], v[42:45], v[166:169], v[18:33]
	v_mfma_f32_32x32x16_bf16 v[2:17], v[46:49], v[166:169], v[2:17]
	s_bitcmp0_b32 s100, 8
	s_cbranch_scc1 .Lstg_a1
	s_waitcnt vmcnt(0)
	s_waitcnt lgkmcnt(0)
	s_barrier

.LBB0_520:
	ds_read_b64_tr_b16 v[144:145], v177 offset:0
	ds_read_b64_tr_b16 v[146:147], v177 offset:0x1000
	ds_read_b64_tr_b16 v[148:149], v177 offset:0x2000
	ds_read_b64_tr_b16 v[150:151], v177 offset:0x3000
	ds_read_b64_tr_b16 v[152:153], v177 offset:0x4000
	ds_read_b64_tr_b16 v[154:155], v177 offset:0x5000
	ds_read_b64_tr_b16 v[156:157], v177 offset:0x6000
	ds_read_b64_tr_b16 v[158:159], v177 offset:0x7000
	ds_read_b64_tr_b16 v[198:199], v177 offset:0x200
	ds_read_b64_tr_b16 v[200:201], v177 offset:0x1200
	ds_read_b64_tr_b16 v[202:203], v177 offset:0x2200
	ds_read_b64_tr_b16 v[204:205], v177 offset:0x3200
	ds_read_b64_tr_b16 v[206:207], v177 offset:0x4200
	ds_read_b64_tr_b16 v[208:209], v177 offset:0x5200
	ds_read_b64_tr_b16 v[210:211], v177 offset:0x6200
	ds_read_b64_tr_b16 v[212:213], v177 offset:0x7200
	s_waitcnt lgkmcnt(8)
	s_nop 0
	v_mfma_f32_32x32x16_bf16 v[112:127], v[144:147], v[128:131], v[112:127]
	v_mfma_f32_32x32x16_bf16 v[112:127], v[148:151], v[132:135], v[112:127]
	v_mfma_f32_32x32x16_bf16 v[112:127], v[152:155], v[136:139], v[112:127]
	v_mfma_f32_32x32x16_bf16 v[112:127], v[156:159], v[140:143], v[112:127]
	ds_read_b64_tr_b16 v[144:145], v177 offset:0x400
	ds_read_b64_tr_b16 v[146:147], v177 offset:0x1400
	ds_read_b64_tr_b16 v[148:149], v177 offset:0x2400
	ds_read_b64_tr_b16 v[150:151], v177 offset:0x3400
	ds_read_b64_tr_b16 v[152:153], v177 offset:0x4400
	ds_read_b64_tr_b16 v[154:155], v177 offset:0x5400
	ds_read_b64_tr_b16 v[156:157], v177 offset:0x6400
	ds_read_b64_tr_b16 v[158:159], v177 offset:0x7400
	s_waitcnt lgkmcnt(8)
	v_mfma_f32_32x32x16_bf16 v[0:15], v[198:201], v[128:131], v[0:15]
	v_mfma_f32_32x32x16_bf16 v[0:15], v[202:205], v[132:135], v[0:15]
	v_mfma_f32_32x32x16_bf16 v[0:15], v[206:209], v[136:139], v[0:15]
	v_mfma_f32_32x32x16_bf16 v[0:15], v[210:213], v[140:143], v[0:15]
	ds_read_b64_tr_b16 v[198:199], v177 offset:0x600
	ds_read_b64_tr_b16 v[200:201], v177 offset:0x1600
	ds_read_b64_tr_b16 v[202:203], v177 offset:0x2600
	ds_read_b64_tr_b16 v[204:205], v177 offset:0x3600
	ds_read_b64_tr_b16 v[206:207], v177 offset:0x4600
	ds_read_b64_tr_b16 v[208:209], v177 offset:0x5600
	ds_read_b64_tr_b16 v[210:211], v177 offset:0x6600
	ds_read_b64_tr_b16 v[212:213], v177 offset:0x7600
	s_waitcnt lgkmcnt(8)
	v_mfma_f32_32x32x16_bf16 v[16:31], v[144:147], v[128:131], v[16:31]
	v_mfma_f32_32x32x16_bf16 v[16:31], v[148:151], v[132:135], v[16:31]
	v_mfma_f32_32x32x16_bf16 v[16:31], v[152:155], v[136:139], v[16:31]
	v_mfma_f32_32x32x16_bf16 v[16:31], v[156:159], v[140:143], v[16:31]
	ds_read_b64_tr_b16 v[144:145], v177 offset:0x800
	ds_read_b64_tr_b16 v[146:147], v177 offset:0x1800
	ds_read_b64_tr_b16 v[148:149], v177 offset:0x2800
	ds_read_b64_tr_b16 v[150:151], v177 offset:0x3800
	ds_read_b64_tr_b16 v[152:153], v177 offset:0x4800
	ds_read_b64_tr_b16 v[154:155], v177 offset:0x5800
	ds_read_b64_tr_b16 v[156:157], v177 offset:0x6800
	ds_read_b64_tr_b16 v[158:159], v177 offset:0x7800
	s_waitcnt lgkmcnt(8)
	v_mfma_f32_32x32x16_bf16 v[32:47], v[198:201], v[128:131], v[32:47]
	v_mfma_f32_32x32x16_bf16 v[32:47], v[202:205], v[132:135], v[32:47]
	v_mfma_f32_32x32x16_bf16 v[32:47], v[206:209], v[136:139], v[32:47]
	v_mfma_f32_32x32x16_bf16 v[32:47], v[210:213], v[140:143], v[32:47]
	ds_read_b64_tr_b16 v[198:199], v177 offset:0xa00
	ds_read_b64_tr_b16 v[200:201], v177 offset:0x1a00
	ds_read_b64_tr_b16 v[202:203], v177 offset:0x2a00
	ds_read_b64_tr_b16 v[204:205], v177 offset:0x3a00
	ds_read_b64_tr_b16 v[206:207], v177 offset:0x4a00
	ds_read_b64_tr_b16 v[208:209], v177 offset:0x5a00
	ds_read_b64_tr_b16 v[210:211], v177 offset:0x6a00
	ds_read_b64_tr_b16 v[212:213], v177 offset:0x7a00
	s_waitcnt lgkmcnt(8)
	v_mfma_f32_32x32x16_bf16 v[48:63], v[144:147], v[128:131], v[48:63]
	v_mfma_f32_32x32x16_bf16 v[48:63], v[148:151], v[132:135], v[48:63]
	v_mfma_f32_32x32x16_bf16 v[48:63], v[152:155], v[136:139], v[48:63]
	v_mfma_f32_32x32x16_bf16 v[48:63], v[156:159], v[140:143], v[48:63]
	ds_read_b64_tr_b16 v[144:145], v177 offset:0xc00
	ds_read_b64_tr_b16 v[146:147], v177 offset:0x1c00
	ds_read_b64_tr_b16 v[148:149], v177 offset:0x2c00
	ds_read_b64_tr_b16 v[150:151], v177 offset:0x3c00
	ds_read_b64_tr_b16 v[152:153], v177 offset:0x4c00
	ds_read_b64_tr_b16 v[154:155], v177 offset:0x5c00
	ds_read_b64_tr_b16 v[156:157], v177 offset:0x6c00
	ds_read_b64_tr_b16 v[158:159], v177 offset:0x7c00
	s_waitcnt lgkmcnt(8)
	v_mfma_f32_32x32x16_bf16 v[64:79], v[198:201], v[128:131], v[64:79]
	v_mfma_f32_32x32x16_bf16 v[64:79], v[202:205], v[132:135], v[64:79]
	v_mfma_f32_32x32x16_bf16 v[64:79], v[206:209], v[136:139], v[64:79]
	v_mfma_f32_32x32x16_bf16 v[64:79], v[210:213], v[140:143], v[64:79]
	ds_read_b64_tr_b16 v[198:199], v177 offset:0xe00
	ds_read_b64_tr_b16 v[200:201], v177 offset:0x1e00
	ds_read_b64_tr_b16 v[202:203], v177 offset:0x2e00
	ds_read_b64_tr_b16 v[204:205], v177 offset:0x3e00
	ds_read_b64_tr_b16 v[206:207], v177 offset:0x4e00
	ds_read_b64_tr_b16 v[208:209], v177 offset:0x5e00
	ds_read_b64_tr_b16 v[210:211], v177 offset:0x6e00
	ds_read_b64_tr_b16 v[212:213], v177 offset:0x7e00
	s_waitcnt lgkmcnt(8)
	v_mfma_f32_32x32x16_bf16 v[80:95], v[144:147], v[128:131], v[80:95]
	v_mfma_f32_32x32x16_bf16 v[80:95], v[148:151], v[132:135], v[80:95]
	v_mfma_f32_32x32x16_bf16 v[80:95], v[152:155], v[136:139], v[80:95]
	v_mfma_f32_32x32x16_bf16 v[80:95], v[156:159], v[140:143], v[80:95]
	s_waitcnt lgkmcnt(0)
	v_mfma_f32_32x32x16_bf16 v[96:111], v[198:201], v[128:131], v[96:111]
	v_mfma_f32_32x32x16_bf16 v[96:111], v[202:205], v[132:135], v[96:111]
	v_mfma_f32_32x32x16_bf16 v[96:111], v[206:209], v[136:139], v[96:111]
	v_mfma_f32_32x32x16_bf16 v[96:111], v[210:213], v[140:143], v[96:111]
	ds_read_b128 v[128:131], v189 offset:0
	ds_read_b128 v[132:135], v189 offset:0x2080
	ds_read_b128 v[136:139], v181 offset:0
	ds_read_b128 v[198:201], v188 offset:0
	ds_read_b128 v[202:205], v188 offset:0x2080
	ds_read_b128 v[206:209], v181 offset:0x400
	s_waitcnt lgkmcnt(3)
	s_nop 0
	v_mfma_f32_32x32x16_bf16 v[144:159], v[128:131], v[136:139], 0
	v_mfma_f32_32x32x16_bf16 v[128:143], v[132:135], v[136:139], 0
	ds_read_b128 v[210:213], v187 offset:0
	ds_read_b128 v[214:217], v187 offset:0x2080
	ds_read_b128 v[218:221], v181 offset:0x800
	s_waitcnt lgkmcnt(3)
	v_mfma_f32_32x32x16_bf16 v[144:159], v[198:201], v[206:209], v[144:159]
	v_mfma_f32_32x32x16_bf16 v[128:143], v[202:205], v[206:209], v[128:143]
	ds_read_b128 v[198:201], v186 offset:0
	ds_read_b128 v[202:205], v186 offset:0x2080
	ds_read_b128 v[206:209], v181 offset:0xc00
	s_waitcnt lgkmcnt(3)
	v_mfma_f32_32x32x16_bf16 v[144:159], v[210:213], v[218:221], v[144:159]
	v_mfma_f32_32x32x16_bf16 v[128:143], v[214:217], v[218:221], v[128:143]
	ds_read_b128 v[210:213], v189 offset:0x80
	ds_read_b128 v[214:217], v189 offset:0x2100
	ds_read_b128 v[218:221], v181 offset:0x1000
	s_waitcnt lgkmcnt(3)
	v_mfma_f32_32x32x16_bf16 v[144:159], v[198:201], v[206:209], v[144:159]
	v_mfma_f32_32x32x16_bf16 v[128:143], v[202:205], v[206:209], v[128:143]
	ds_read_b128 v[198:201], v188 offset:0x80
	ds_read_b128 v[202:205], v188 offset:0x2100
	ds_read_b128 v[206:209], v181 offset:0x1400
	s_waitcnt lgkmcnt(3)
	v_mfma_f32_32x32x16_bf16 v[144:159], v[210:213], v[218:221], v[144:159]
	v_mfma_f32_32x32x16_bf16 v[128:143], v[214:217], v[218:221], v[128:143]
	ds_read_b128 v[210:213], v187 offset:0x80
	ds_read_b128 v[214:217], v187 offset:0x2100
	ds_read_b128 v[218:221], v181 offset:0x1800
	s_waitcnt lgkmcnt(3)
	v_mfma_f32_32x32x16_bf16 v[144:159], v[198:201], v[206:209], v[144:159]
	v_mfma_f32_32x32x16_bf16 v[128:143], v[202:205], v[206:209], v[128:143]
	ds_read_b128 v[198:201], v186 offset:0x80
	ds_read_b128 v[202:205], v186 offset:0x2100
	s_waitcnt lgkmcnt(2)
	v_mfma_f32_32x32x16_bf16 v[144:159], v[210:213], v[218:221], v[144:159]
	v_mfma_f32_32x32x16_bf16 v[128:143], v[214:217], v[218:221], v[128:143]
	s_waitcnt lgkmcnt(0)
	v_mfma_f32_32x32x16_bf16 v[144:159], v[198:201], v[166:169], v[144:159]
	v_mfma_f32_32x32x16_bf16 v[128:143], v[202:205], v[166:169], v[128:143]
	s_bitcmp0_b32 s100, 8
	s_cbranch_scc1 .Lstg_a2
	s_waitcnt vmcnt(0)
	s_waitcnt lgkmcnt(0)
	s_barrier

.LBB0_526:
	s_add_u32 s33, s72, s84
	s_addc_u32 s92, s73, s90
	s_add_u32 s4, s33, 0x2dd40800
	s_addc_u32 s5, s92, 0
	s_mov_b32 m0, s81
	s_nop 0
	global_load_lds_dwordx4 v162, s[4:5]
	s_add_i32 m0, s78, 0xffffff80
	s_nop 0
	global_load_lds_dwordx4 v162, s[4:5] offset:128
	s_add_i32 m0, s69, 0xffffff00
	s_nop 0
	global_load_lds_dwordx4 v162, s[4:5] offset:256
	s_add_i32 m0, s68, 0xfffffe80
	s_nop 0
	global_load_lds_dwordx4 v162, s[4:5] offset:384
	ds_read_b64_tr_b16 v[144:145], v177 offset:0x8000
	ds_read_b64_tr_b16 v[146:147], v177 offset:0x9000
	ds_read_b64_tr_b16 v[148:149], v177 offset:0xa000
	ds_read_b64_tr_b16 v[150:151], v177 offset:0xb000
	ds_read_b64_tr_b16 v[152:153], v177 offset:0xc000
	ds_read_b64_tr_b16 v[154:155], v177 offset:0xd000
	ds_read_b64_tr_b16 v[156:157], v177 offset:0xe000
	ds_read_b64_tr_b16 v[158:159], v177 offset:0xf000
	ds_read_b64_tr_b16 v[236:237], v177 offset:0x8200
	ds_read_b64_tr_b16 v[238:239], v177 offset:0x9200
	ds_read_b64_tr_b16 v[240:241], v177 offset:0xa200
	ds_read_b64_tr_b16 v[242:243], v177 offset:0xb200
	ds_read_b64_tr_b16 v[244:245], v177 offset:0xc200
	ds_read_b64_tr_b16 v[246:247], v177 offset:0xd200
	ds_read_b64_tr_b16 v[248:249], v177 offset:0xe200
	ds_read_b64_tr_b16 v[250:251], v177 offset:0xf200
	s_waitcnt lgkmcnt(8)
	s_nop 1
	v_mfma_f32_32x32x16_bf16 v[112:127], v[144:147], v[128:131], v[112:127]
	v_mfma_f32_32x32x16_bf16 v[112:127], v[148:151], v[132:135], v[112:127]
	v_mfma_f32_32x32x16_bf16 v[112:127], v[152:155], v[136:139], v[112:127]
	v_mfma_f32_32x32x16_bf16 v[112:127], v[156:159], v[140:143], v[112:127]
	ds_read_b64_tr_b16 v[144:145], v177 offset:0x8400
	ds_read_b64_tr_b16 v[146:147], v177 offset:0x9400
	ds_read_b64_tr_b16 v[148:149], v177 offset:0xa400
	ds_read_b64_tr_b16 v[150:151], v177 offset:0xb400
	ds_read_b64_tr_b16 v[152:153], v177 offset:0xc400
	ds_read_b64_tr_b16 v[154:155], v177 offset:0xd400
	ds_read_b64_tr_b16 v[156:157], v177 offset:0xe400
	ds_read_b64_tr_b16 v[158:159], v177 offset:0xf400
	s_waitcnt lgkmcnt(8)
	v_mfma_f32_32x32x16_bf16 v[0:15], v[236:239], v[128:131], v[0:15]
	v_mfma_f32_32x32x16_bf16 v[0:15], v[240:243], v[132:135], v[0:15]
	v_mfma_f32_32x32x16_bf16 v[0:15], v[244:247], v[136:139], v[0:15]
	v_mfma_f32_32x32x16_bf16 v[0:15], v[248:251], v[140:143], v[0:15]
	ds_read_b64_tr_b16 v[236:237], v177 offset:0x8600
	ds_read_b64_tr_b16 v[238:239], v177 offset:0x9600
	ds_read_b64_tr_b16 v[240:241], v177 offset:0xa600
	ds_read_b64_tr_b16 v[242:243], v177 offset:0xb600
	ds_read_b64_tr_b16 v[244:245], v177 offset:0xc600
	ds_read_b64_tr_b16 v[246:247], v177 offset:0xd600
	ds_read_b64_tr_b16 v[248:249], v177 offset:0xe600
	ds_read_b64_tr_b16 v[250:251], v177 offset:0xf600
	s_waitcnt lgkmcnt(8)
	v_mfma_f32_32x32x16_bf16 v[16:31], v[144:147], v[128:131], v[16:31]
	v_mfma_f32_32x32x16_bf16 v[16:31], v[148:151], v[132:135], v[16:31]
	v_mfma_f32_32x32x16_bf16 v[16:31], v[152:155], v[136:139], v[16:31]
	v_mfma_f32_32x32x16_bf16 v[16:31], v[156:159], v[140:143], v[16:31]
	ds_read_b64_tr_b16 v[144:145], v177 offset:0x8800
	ds_read_b64_tr_b16 v[146:147], v177 offset:0x9800
	ds_read_b64_tr_b16 v[148:149], v177 offset:0xa800
	ds_read_b64_tr_b16 v[150:151], v177 offset:0xb800
	ds_read_b64_tr_b16 v[152:153], v177 offset:0xc800
	ds_read_b64_tr_b16 v[154:155], v177 offset:0xd800
	ds_read_b64_tr_b16 v[156:157], v177 offset:0xe800
	ds_read_b64_tr_b16 v[158:159], v177 offset:0xf800
	s_waitcnt lgkmcnt(8)
	v_mfma_f32_32x32x16_bf16 v[32:47], v[236:239], v[128:131], v[32:47]
	v_mfma_f32_32x32x16_bf16 v[32:47], v[240:243], v[132:135], v[32:47]
	v_mfma_f32_32x32x16_bf16 v[32:47], v[244:247], v[136:139], v[32:47]
	v_mfma_f32_32x32x16_bf16 v[32:47], v[248:251], v[140:143], v[32:47]
	ds_read_b64_tr_b16 v[236:237], v177 offset:0x8a00
	ds_read_b64_tr_b16 v[238:239], v177 offset:0x9a00
	ds_read_b64_tr_b16 v[240:241], v177 offset:0xaa00
	ds_read_b64_tr_b16 v[242:243], v177 offset:0xba00
	ds_read_b64_tr_b16 v[244:245], v177 offset:0xca00
	ds_read_b64_tr_b16 v[246:247], v177 offset:0xda00
	ds_read_b64_tr_b16 v[248:249], v177 offset:0xea00
	ds_read_b64_tr_b16 v[250:251], v177 offset:0xfa00
	s_waitcnt lgkmcnt(8)
	v_mfma_f32_32x32x16_bf16 v[48:63], v[144:147], v[128:131], v[48:63]
	v_mfma_f32_32x32x16_bf16 v[48:63], v[148:151], v[132:135], v[48:63]
	v_mfma_f32_32x32x16_bf16 v[48:63], v[152:155], v[136:139], v[48:63]
	v_mfma_f32_32x32x16_bf16 v[48:63], v[156:159], v[140:143], v[48:63]
	ds_read_b64_tr_b16 v[144:145], v177 offset:0x8c00
	ds_read_b64_tr_b16 v[146:147], v177 offset:0x9c00
	ds_read_b64_tr_b16 v[148:149], v177 offset:0xac00
	ds_read_b64_tr_b16 v[150:151], v177 offset:0xbc00
	ds_read_b64_tr_b16 v[152:153], v177 offset:0xcc00
	ds_read_b64_tr_b16 v[154:155], v177 offset:0xdc00
	ds_read_b64_tr_b16 v[156:157], v177 offset:0xec00
	ds_read_b64_tr_b16 v[158:159], v177 offset:0xfc00
	s_waitcnt lgkmcnt(8)
	v_mfma_f32_32x32x16_bf16 v[64:79], v[236:239], v[128:131], v[64:79]
	v_mfma_f32_32x32x16_bf16 v[64:79], v[240:243], v[132:135], v[64:79]
	v_mfma_f32_32x32x16_bf16 v[64:79], v[244:247], v[136:139], v[64:79]
	v_mfma_f32_32x32x16_bf16 v[64:79], v[248:251], v[140:143], v[64:79]
	ds_read_b64_tr_b16 v[236:237], v177 offset:0x8e00
	ds_read_b64_tr_b16 v[238:239], v177 offset:0x9e00
	ds_read_b64_tr_b16 v[240:241], v177 offset:0xae00
	ds_read_b64_tr_b16 v[242:243], v177 offset:0xbe00
	ds_read_b64_tr_b16 v[244:245], v177 offset:0xce00
	ds_read_b64_tr_b16 v[246:247], v177 offset:0xde00
	ds_read_b64_tr_b16 v[248:249], v177 offset:0xee00
	ds_read_b64_tr_b16 v[250:251], v177 offset:0xfe00
	s_waitcnt lgkmcnt(8)
	v_mfma_f32_32x32x16_bf16 v[80:95], v[144:147], v[128:131], v[80:95]
	v_mfma_f32_32x32x16_bf16 v[80:95], v[148:151], v[132:135], v[80:95]
	v_mfma_f32_32x32x16_bf16 v[80:95], v[152:155], v[136:139], v[80:95]
	v_mfma_f32_32x32x16_bf16 v[80:95], v[156:159], v[140:143], v[80:95]
	s_waitcnt lgkmcnt(0)
	v_mfma_f32_32x32x16_bf16 v[96:111], v[236:239], v[128:131], v[96:111]
	v_mfma_f32_32x32x16_bf16 v[96:111], v[240:243], v[132:135], v[96:111]
	v_mfma_f32_32x32x16_bf16 v[96:111], v[244:247], v[136:139], v[96:111]
	v_mfma_f32_32x32x16_bf16 v[96:111], v[248:251], v[140:143], v[96:111]
	ds_read_b128 v[128:131], v182 offset:0
	ds_read_b128 v[132:135], v182 offset:0x2080
	ds_read_b128 v[136:139], v181 offset:0
	ds_read_b128 v[236:239], v183 offset:0
	ds_read_b128 v[240:243], v183 offset:0x2080
	ds_read_b128 v[244:247], v181 offset:0x400
	s_waitcnt lgkmcnt(3)
	s_nop 0
	v_mfma_f32_32x32x16_bf16 v[144:159], v[128:131], v[136:139], 0
	v_mfma_f32_32x32x16_bf16 v[128:143], v[132:135], v[136:139], 0
	ds_read_b128 v[248:251], v184 offset:0
	ds_read_b128 v[194:197], v184 offset:0x2080
	ds_read_b128 v[222:225], v181 offset:0x800
	s_waitcnt lgkmcnt(3)
	v_mfma_f32_32x32x16_bf16 v[144:159], v[236:239], v[244:247], v[144:159]
	v_mfma_f32_32x32x16_bf16 v[128:143], v[240:243], v[244:247], v[128:143]
	ds_read_b128 v[236:239], v185 offset:0
	ds_read_b128 v[240:243], v185 offset:0x2080
	ds_read_b128 v[244:247], v181 offset:0xc00
	s_waitcnt lgkmcnt(3)
	v_mfma_f32_32x32x16_bf16 v[144:159], v[248:251], v[222:225], v[144:159]
	v_mfma_f32_32x32x16_bf16 v[128:143], v[194:197], v[222:225], v[128:143]
	ds_read_b128 v[194:197], v182 offset:0x80
	ds_read_b128 v[222:225], v182 offset:0x2100
	ds_read_b128 v[248:251], v181 offset:0x1000
	s_waitcnt lgkmcnt(3)
	v_mfma_f32_32x32x16_bf16 v[144:159], v[236:239], v[244:247], v[144:159]
	v_mfma_f32_32x32x16_bf16 v[128:143], v[240:243], v[244:247], v[128:143]
	ds_read_b128 v[236:239], v183 offset:0x80
	ds_read_b128 v[240:243], v183 offset:0x2100
	ds_read_b128 v[244:247], v181 offset:0x1400
	s_waitcnt lgkmcnt(3)
	v_mfma_f32_32x32x16_bf16 v[144:159], v[194:197], v[248:251], v[144:159]
	v_mfma_f32_32x32x16_bf16 v[128:143], v[222:225], v[248:251], v[128:143]
	ds_read_b128 v[194:197], v184 offset:0x80
	ds_read_b128 v[222:225], v184 offset:0x2100
	ds_read_b128 v[248:251], v181 offset:0x1800
	s_waitcnt lgkmcnt(3)
	v_mfma_f32_32x32x16_bf16 v[144:159], v[236:239], v[244:247], v[144:159]
	v_mfma_f32_32x32x16_bf16 v[128:143], v[240:243], v[244:247], v[128:143]
	ds_read_b128 v[236:239], v185 offset:0x80
	ds_read_b128 v[240:243], v185 offset:0x2100
	s_waitcnt lgkmcnt(2)
	v_mfma_f32_32x32x16_bf16 v[144:159], v[194:197], v[248:251], v[144:159]
	v_mfma_f32_32x32x16_bf16 v[128:143], v[222:225], v[248:251], v[128:143]
	s_waitcnt lgkmcnt(0)
	v_mfma_f32_32x32x16_bf16 v[144:159], v[236:239], v[166:169], v[144:159]
	v_mfma_f32_32x32x16_bf16 v[128:143], v[240:243], v[166:169], v[128:143]
	s_bitcmp0_b32 s100, 8
	s_cbranch_scc1 .Lstg_a3
	s_waitcnt vmcnt(0)
	s_waitcnt lgkmcnt(0)
	s_barrier

.LBB0_539:
	ds_read_b64_tr_b16 v[144:145], v177 offset:0
	ds_read_b64_tr_b16 v[146:147], v177 offset:0x1000
	ds_read_b64_tr_b16 v[148:149], v177 offset:0x2000
	ds_read_b64_tr_b16 v[150:151], v177 offset:0x3000
	ds_read_b64_tr_b16 v[152:153], v177 offset:0x4000
	ds_read_b64_tr_b16 v[154:155], v177 offset:0x5000
	ds_read_b64_tr_b16 v[156:157], v177 offset:0x6000
	ds_read_b64_tr_b16 v[158:159], v177 offset:0x7000
	ds_read_b64_tr_b16 v[170:171], v177 offset:0x200
	ds_read_b64_tr_b16 v[172:173], v177 offset:0x1200
	ds_read_b64_tr_b16 v[182:183], v177 offset:0x2200
	ds_read_b64_tr_b16 v[184:185], v177 offset:0x3200
	ds_read_b64_tr_b16 v[190:191], v177 offset:0x4200
	ds_read_b64_tr_b16 v[192:193], v177 offset:0x5200
	ds_read_b64_tr_b16 v[198:199], v177 offset:0x6200
	ds_read_b64_tr_b16 v[200:201], v177 offset:0x7200
	s_waitcnt lgkmcnt(8)
	s_nop 0
	v_mfma_f32_32x32x16_bf16 v[112:127], v[144:147], v[128:131], v[112:127]
	v_mfma_f32_32x32x16_bf16 v[112:127], v[148:151], v[132:135], v[112:127]
	v_mfma_f32_32x32x16_bf16 v[112:127], v[152:155], v[136:139], v[112:127]
	v_mfma_f32_32x32x16_bf16 v[112:127], v[156:159], v[140:143], v[112:127]
	ds_read_b64_tr_b16 v[144:145], v177 offset:0x400
	ds_read_b64_tr_b16 v[146:147], v177 offset:0x1400
	ds_read_b64_tr_b16 v[148:149], v177 offset:0x2400
	ds_read_b64_tr_b16 v[150:151], v177 offset:0x3400
	ds_read_b64_tr_b16 v[152:153], v177 offset:0x4400
	ds_read_b64_tr_b16 v[154:155], v177 offset:0x5400
	ds_read_b64_tr_b16 v[156:157], v177 offset:0x6400
	ds_read_b64_tr_b16 v[158:159], v177 offset:0x7400
	s_waitcnt lgkmcnt(8)
	v_mfma_f32_32x32x16_bf16 v[0:15], v[170:173], v[128:131], v[0:15]
	v_mfma_f32_32x32x16_bf16 v[0:15], v[182:185], v[132:135], v[0:15]
	v_mfma_f32_32x32x16_bf16 v[0:15], v[190:193], v[136:139], v[0:15]
	v_mfma_f32_32x32x16_bf16 v[0:15], v[198:201], v[140:143], v[0:15]
	ds_read_b64_tr_b16 v[170:171], v177 offset:0x600
	ds_read_b64_tr_b16 v[172:173], v177 offset:0x1600
	ds_read_b64_tr_b16 v[182:183], v177 offset:0x2600
	ds_read_b64_tr_b16 v[184:185], v177 offset:0x3600
	ds_read_b64_tr_b16 v[190:191], v177 offset:0x4600
	ds_read_b64_tr_b16 v[192:193], v177 offset:0x5600
	ds_read_b64_tr_b16 v[198:199], v177 offset:0x6600
	ds_read_b64_tr_b16 v[200:201], v177 offset:0x7600
	s_waitcnt lgkmcnt(8)
	v_mfma_f32_32x32x16_bf16 v[16:31], v[144:147], v[128:131], v[16:31]
	v_mfma_f32_32x32x16_bf16 v[16:31], v[148:151], v[132:135], v[16:31]
	v_mfma_f32_32x32x16_bf16 v[16:31], v[152:155], v[136:139], v[16:31]
	v_mfma_f32_32x32x16_bf16 v[16:31], v[156:159], v[140:143], v[16:31]
	ds_read_b64_tr_b16 v[144:145], v177 offset:0x800
	ds_read_b64_tr_b16 v[146:147], v177 offset:0x1800
	ds_read_b64_tr_b16 v[148:149], v177 offset:0x2800
	ds_read_b64_tr_b16 v[150:151], v177 offset:0x3800
	ds_read_b64_tr_b16 v[152:153], v177 offset:0x4800
	ds_read_b64_tr_b16 v[154:155], v177 offset:0x5800
	ds_read_b64_tr_b16 v[156:157], v177 offset:0x6800
	ds_read_b64_tr_b16 v[158:159], v177 offset:0x7800
	s_waitcnt lgkmcnt(8)
	v_mfma_f32_32x32x16_bf16 v[32:47], v[170:173], v[128:131], v[32:47]
	v_mfma_f32_32x32x16_bf16 v[32:47], v[182:185], v[132:135], v[32:47]
	v_mfma_f32_32x32x16_bf16 v[32:47], v[190:193], v[136:139], v[32:47]
	v_mfma_f32_32x32x16_bf16 v[32:47], v[198:201], v[140:143], v[32:47]
	ds_read_b64_tr_b16 v[170:171], v177 offset:0xa00
	ds_read_b64_tr_b16 v[172:173], v177 offset:0x1a00
	ds_read_b64_tr_b16 v[182:183], v177 offset:0x2a00
	ds_read_b64_tr_b16 v[184:185], v177 offset:0x3a00
	ds_read_b64_tr_b16 v[190:191], v177 offset:0x4a00
	ds_read_b64_tr_b16 v[192:193], v177 offset:0x5a00
	ds_read_b64_tr_b16 v[198:199], v177 offset:0x6a00
	ds_read_b64_tr_b16 v[200:201], v177 offset:0x7a00
	s_waitcnt lgkmcnt(8)
	v_mfma_f32_32x32x16_bf16 v[48:63], v[144:147], v[128:131], v[48:63]
	v_mfma_f32_32x32x16_bf16 v[48:63], v[148:151], v[132:135], v[48:63]
	v_mfma_f32_32x32x16_bf16 v[48:63], v[152:155], v[136:139], v[48:63]
	v_mfma_f32_32x32x16_bf16 v[48:63], v[156:159], v[140:143], v[48:63]
	ds_read_b64_tr_b16 v[144:145], v177 offset:0xc00
	ds_read_b64_tr_b16 v[146:147], v177 offset:0x1c00
	ds_read_b64_tr_b16 v[148:149], v177 offset:0x2c00
	ds_read_b64_tr_b16 v[150:151], v177 offset:0x3c00
	ds_read_b64_tr_b16 v[152:153], v177 offset:0x4c00
	ds_read_b64_tr_b16 v[154:155], v177 offset:0x5c00
	ds_read_b64_tr_b16 v[156:157], v177 offset:0x6c00
	ds_read_b64_tr_b16 v[158:159], v177 offset:0x7c00
	s_waitcnt lgkmcnt(8)
	v_mfma_f32_32x32x16_bf16 v[64:79], v[170:173], v[128:131], v[64:79]
	v_mfma_f32_32x32x16_bf16 v[64:79], v[182:185], v[132:135], v[64:79]
	v_mfma_f32_32x32x16_bf16 v[64:79], v[190:193], v[136:139], v[64:79]
	v_mfma_f32_32x32x16_bf16 v[64:79], v[198:201], v[140:143], v[64:79]
	ds_read_b64_tr_b16 v[170:171], v177 offset:0xe00
	ds_read_b64_tr_b16 v[172:173], v177 offset:0x1e00
	ds_read_b64_tr_b16 v[182:183], v177 offset:0x2e00
	ds_read_b64_tr_b16 v[184:185], v177 offset:0x3e00
	ds_read_b64_tr_b16 v[190:191], v177 offset:0x4e00
	ds_read_b64_tr_b16 v[192:193], v177 offset:0x5e00
	ds_read_b64_tr_b16 v[198:199], v177 offset:0x6e00
	ds_read_b64_tr_b16 v[200:201], v177 offset:0x7e00
	s_waitcnt lgkmcnt(8)
	v_mfma_f32_32x32x16_bf16 v[80:95], v[144:147], v[128:131], v[80:95]
	v_mfma_f32_32x32x16_bf16 v[80:95], v[148:151], v[132:135], v[80:95]
	v_mfma_f32_32x32x16_bf16 v[80:95], v[152:155], v[136:139], v[80:95]
	v_mfma_f32_32x32x16_bf16 v[80:95], v[156:159], v[140:143], v[80:95]
	s_waitcnt lgkmcnt(0)
	v_mfma_f32_32x32x16_bf16 v[96:111], v[170:173], v[128:131], v[96:111]
	v_mfma_f32_32x32x16_bf16 v[96:111], v[182:185], v[132:135], v[96:111]
	v_mfma_f32_32x32x16_bf16 v[96:111], v[190:193], v[136:139], v[96:111]
	v_mfma_f32_32x32x16_bf16 v[96:111], v[198:201], v[140:143], v[96:111]
	ds_read_b128 v[128:131], v189 offset:0
	ds_read_b128 v[132:135], v189 offset:0x2080
	ds_read_b128 v[136:139], v181 offset:0
	ds_read_b128 v[170:173], v188 offset:0
	ds_read_b128 v[182:185], v188 offset:0x2080
	ds_read_b128 v[190:193], v181 offset:0x400
	s_waitcnt lgkmcnt(3)
	s_nop 0
	v_mfma_f32_32x32x16_bf16 v[144:159], v[128:131], v[136:139], 0
	v_mfma_f32_32x32x16_bf16 v[128:143], v[132:135], v[136:139], 0
	ds_read_b128 v[198:201], v187 offset:0
	ds_read_b128 v[202:205], v187 offset:0x2080
	ds_read_b128 v[206:209], v181 offset:0x800
	s_waitcnt lgkmcnt(3)
	v_mfma_f32_32x32x16_bf16 v[144:159], v[170:173], v[190:193], v[144:159]
	v_mfma_f32_32x32x16_bf16 v[128:143], v[182:185], v[190:193], v[128:143]
	ds_read_b128 v[170:173], v186 offset:0
	ds_read_b128 v[182:185], v186 offset:0x2080
	ds_read_b128 v[190:193], v181 offset:0xc00
	s_waitcnt lgkmcnt(3)
	v_mfma_f32_32x32x16_bf16 v[144:159], v[198:201], v[206:209], v[144:159]
	v_mfma_f32_32x32x16_bf16 v[128:143], v[202:205], v[206:209], v[128:143]
	ds_read_b128 v[198:201], v189 offset:0x80
	ds_read_b128 v[202:205], v189 offset:0x2100
	ds_read_b128 v[206:209], v181 offset:0x1000
	s_waitcnt lgkmcnt(3)
	v_mfma_f32_32x32x16_bf16 v[144:159], v[170:173], v[190:193], v[144:159]
	v_mfma_f32_32x32x16_bf16 v[128:143], v[182:185], v[190:193], v[128:143]
	ds_read_b128 v[170:173], v188 offset:0x80
	ds_read_b128 v[182:185], v188 offset:0x2100
	ds_read_b128 v[188:191], v181 offset:0x1400
	s_waitcnt lgkmcnt(3)
	v_mfma_f32_32x32x16_bf16 v[144:159], v[198:201], v[206:209], v[144:159]
	v_mfma_f32_32x32x16_bf16 v[128:143], v[202:205], v[206:209], v[128:143]
	ds_read_b128 v[198:201], v187 offset:0x80
	ds_read_b128 v[202:205], v187 offset:0x2100
	ds_read_b128 v[206:209], v181 offset:0x1800
	s_waitcnt lgkmcnt(3)
	v_mfma_f32_32x32x16_bf16 v[144:159], v[170:173], v[188:191], v[144:159]
	v_mfma_f32_32x32x16_bf16 v[128:143], v[182:185], v[188:191], v[128:143]
	ds_read_b128 v[170:173], v186 offset:0x80
	ds_read_b128 v[182:185], v186 offset:0x2100
	s_waitcnt lgkmcnt(2)
	v_mfma_f32_32x32x16_bf16 v[144:159], v[198:201], v[206:209], v[144:159]
	v_mfma_f32_32x32x16_bf16 v[128:143], v[202:205], v[206:209], v[128:143]
	s_waitcnt lgkmcnt(0)
	v_mfma_f32_32x32x16_bf16 v[144:159], v[170:173], v[166:169], v[144:159]
	v_mfma_f32_32x32x16_bf16 v[128:143], v[182:185], v[166:169], v[128:143]
	s_bitcmp0_b32 s100, 8
	s_cbranch_scc1 .Lstg_a4
	s_waitcnt vmcnt(0)
	s_waitcnt lgkmcnt(0)
	s_barrier

.LBB0_549:
	s_add_i32 s0, s77, 0x26b28
	v_mov_b32_e32 v6, s0
	s_add_i32 s0, s77, 0x26b2c
	v_mov_b32_e32 v7, s0
	ds_read_b32 v6, v6
	ds_read_b32 v7, v7
	s_cmp_lg_u32 s4, 0
	s_waitcnt lgkmcnt(1)
	v_readfirstlane_b32 s1, v6
	s_waitcnt lgkmcnt(0)
	v_readfirstlane_b32 s0, v7
	s_cbranch_scc0 .LBB0_617
	v_writelane_b32 v255, s70, 23
	s_lshl_b32 s4, s4, 2
	v_lshlrev_b32_e32 v160, 4, v5
	v_writelane_b32 v255, s71, 24
	v_writelane_b32 v255, s4, 20
	s_add_u32 s4, s3, 0x1da00000
	v_writelane_b32 v255, s4, 43
	s_addc_u32 s4, s2, 0
	v_writelane_b32 v255, s4, 44
	s_add_u32 s9, s3, 0x2da00000
	v_readlane_b32 s16, v255, 6
	v_readlane_b32 s17, v255, 7
	s_addc_u32 s10, s2, 0
	s_lshl_b64 s[4:5], s[16:17], 10
	s_add_u32 s4, s1, s4
	s_addc_u32 s5, s0, s5
	s_waitcnt vmcnt(0) lgkmcnt(0)
	s_barrier
	v_lshl_add_u64 v[6:7], s[4:5], 0, v[160:161]
	flat_load_dwordx4 v[6:9], v[6:7]
	v_readlane_b32 s1, v255, 18
	s_lshl_b32 s0, s1, 6
	s_lshl_b32 s1, s1, 8
	s_and_b32 s4, s0, 0xfffff000
	s_and_b32 s1, s1, 0x700
	s_or_b32 s1, s1, s4
	s_xor_b32 s1, s1, 0xf00
	s_mul_hi_i32 s7, s1, 0x6800
	s_mulk_i32 s1, 0x6800
	s_add_u32 s1, s9, s1
	s_addc_u32 s7, s10, s7
	s_and_b32 s0, s0, 0xe00
	s_add_u32 s8, s1, s0
	s_mul_hi_i32 s5, s4, 0x6800
	s_mulk_i32 s4, 0x6800
	s_addc_u32 s7, s7, 0
	s_add_u32 s1, s9, s4
	s_addc_u32 s4, s10, s5
	s_add_u32 s5, s1, s0
	v_writelane_b32 v255, s9, 21
	s_addc_u32 s9, s4, 0
	s_add_u32 s0, s5, 0x2800
	v_add_u32_e32 v165, s67, v0
	s_addc_u32 s1, s9, 0
	v_readfirstlane_b32 s6, v165
	s_add_u32 s4, s5, 0x3800
	v_and_b32_e32 v10, 31, v0
	s_addc_u32 s5, s9, 0
	s_ashr_i32 s6, s6, 6
	v_lshrrev_b32_e32 v12, 1, v0
	v_lshrrev_b32_e32 v5, 4, v5
	v_and_b32_e32 v14, 15, v0
	v_bfe_u32 v17, v0, 2, 3
	v_lshlrev_b32_e32 v16, 3, v0
	v_mul_u32_u24_e32 v10, 0x6800, v10
	v_writelane_b32 v255, s10, 22
	s_lshl_b32 s9, s6, 3
	s_lshl_b32 s10, s6, 2
	v_and_b32_e32 v18, 32, v0
	v_bitop3_b32 v0, v5, v0, 15 bitop3:0x78
	v_bitop3_b32 v14, v5, v14, 4 bitop3:0x36
	v_and_b32_e32 v19, 8, v12
	v_and_b32_e32 v20, 24, v16
	v_and_or_b32 v16, v12, 16, v10
	v_or_b32_e32 v5, s9, v5
	v_bitop3_b32 v10, s9, v228, v17 bitop3:0xc8
	s_and_b32 s9, s10, 4
	v_mul_lo_u32 v5, v5, s84
	v_or3_b32 v12, v19, v10, s9
	v_lshl_or_b32 v10, v0, 4, v5
	v_lshl_or_b32 v0, v14, 4, v5
	v_mul_u32_u24_e32 v5, 0x3400, v12
	s_add_i32 s13, s77, 0x18300
	v_add_u32_e32 v12, 0x1a000, v0
	v_or3_b32 v0, v18, v20, v5
	v_mov_b32_e32 v11, v161
	v_mov_b32_e32 v13, v161
	v_mov_b32_e32 v15, v161
	v_add_u32_e32 v24, s13, v160
	v_lshlrev_b32_e32 v14, 1, v0
	s_add_i32 s14, s77, 0x10000
	s_lshl_b32 s11, s6, 11
	v_lshl_add_u64 v[10:11], s[0:1], 0, v[10:11]
	v_lshl_add_u64 v[12:13], s[0:1], 0, v[12:13]
	v_lshl_add_u64 v[14:15], s[4:5], 0, v[14:15]
	s_mov_b64 s[0:1], 0x180
	s_add_i32 s10, s11, s14
	s_add_i32 s98, s6, 2
	s_lshr_b32 s98, s98, 2
	s_lshl_b32 s98, s98, 7
	s_add_i32 s10, s10, s98
	v_lshl_add_u64 v[22:23], v[14:15], 0, s[0:1]
	s_lshl_b32 s12, s6, 12
	s_add_i32 s9, s10, 0x400
	v_writelane_b32 v255, s13, 28
	s_lshl_b32 s13, s6, 5
	s_add_i32 s11, s12, s77
	s_mul_hi_i32 s12, s13, 0x6800
	s_add_i32 s13, s11, 0x400
	v_lshl_add_u64 v[18:19], v[14:15], 0, s[86:87]
	v_writelane_b32 v255, s14, 53
	s_add_i32 s14, s11, 0x800
	v_lshl_add_u64 v[20:21], v[14:15], 0, s[62:63]
	s_waitcnt vmcnt(0) lgkmcnt(0)
	ds_write_b128 v24, v[6:9]
	s_mov_b32 s0, m0
	s_mov_b32 m0, s10
	s_nop 0
	global_load_lds_dwordx4 v[10:11], off
	s_mov_b32 m0, s0
	s_mul_i32 s6, s6, 0xd0000
	s_mov_b32 s0, m0
	s_mov_b32 m0, s9
	s_nop 0
	global_load_lds_dwordx4 v[12:13], off
	s_mov_b32 m0, s0
	s_add_i32 s15, s11, 0xc00
	s_mov_b32 s0, m0
	s_mov_b32 m0, s11
	s_nop 0
	global_load_lds_dwordx4 v[14:15], off
	s_mov_b32 m0, s0
	v_mov_b32_e32 v17, v161
	s_mov_b32 s0, m0
	s_mov_b32 m0, s13
	s_nop 0
	global_load_lds_dwordx4 v[18:19], off
	s_mov_b32 m0, s0
	v_cvt_f32_u32_e32 v0, s16
	s_mov_b32 s0, m0
	s_mov_b32 m0, s14
	s_nop 0
	global_load_lds_dwordx4 v[20:21], off
	s_mov_b32 m0, s0
	s_mov_b64 s[80:81], src_shared_base
	s_mov_b32 s0, m0
	s_mov_b32 m0, s15
	s_nop 0
	global_load_lds_dwordx4 v[22:23], off
	s_mov_b32 m0, s0
	s_add_u32 s0, s8, s6
	s_addc_u32 s1, s7, s12
	s_add_u32 s0, s0, 0x1800
	s_addc_u32 s1, s1, 0
	v_lshl_add_u64 v[6:7], s[0:1], 0, v[16:17]
	flat_load_dwordx4 v[128:131], v[6:7]
	flat_load_dwordx4 v[132:135], v[6:7] offset:32
	flat_load_dwordx4 v[136:139], v[6:7] offset:64
	flat_load_dwordx4 v[140:143], v[6:7] offset:96
	flat_load_dwordx4 v[144:147], v[6:7] offset:128
	flat_load_dwordx4 v[148:151], v[6:7] offset:160
	flat_load_dwordx4 v[152:155], v[6:7] offset:192
	flat_load_dwordx4 v[166:169], v[6:7] offset:224
	v_cmp_eq_u32_e64 s[0:1], 0, v165
	s_add_i32 s4, s77, 0x18800
	s_mov_b32 s5, s81
	v_writelane_b32 v255, s0, 49
	v_mul_f32_e32 v0, 0xbe99999a, v0
	v_mul_f32_e32 v0, 0x3fb8aa3b, v0
	v_writelane_b32 v255, s1, 50
	v_writelane_b32 v255, s4, 46
	v_exp_f32_e32 v0, v0
	v_add_f32_e32 v1, v1, v3
	v_writelane_b32 v255, s5, 47
	s_add_i32 s4, s77, 0x18820
	v_add_f32_e32 v2, v2, v4
	v_writelane_b32 v255, s4, 51
	s_add_i32 s4, s77, 0x14100
	v_mul_f32_e32 v1, 0x3fb8aa3b, v1
	v_mul_f32_e32 v2, 0x3fb8aa3b, v2
	v_writelane_b32 v255, s4, 56
	s_add_i32 s4, s77, 0x18804
	s_mov_b32 s5, s81
	v_exp_f32_e32 v1, v1
	v_exp_f32_e32 v2, v2
	s_add_i32 s0, s77, 0x18810
	s_add_i32 s80, s77, 0x18808
	s_add_i32 s72, s77, 0x1880c
	s_add_i32 s70, s77, 0x18814
	v_writelane_b32 v255, s4, 54
	v_mov_b32_e32 v3, 0xbf4ccccd
	s_add_u32 s3, s3, 0x2dd43800
	v_writelane_b32 v255, s5, 55
	v_fmamk_f32 v0, v0, 0x3f19999a, v3
	v_writelane_b32 v255, s3, 27
	s_addc_u32 s2, s2, 0
	v_add_f32_e32 v173, 1.0, v0
	v_writelane_b32 v255, s2, 29
	v_sub_f32_e32 v0, v1, v2
	v_sub_f32_e32 v1, 1.0, v173
	v_writelane_b32 v255, s77, 48
	v_add_f32_e32 v174, v1, v0
	s_mov_b32 s94, 0
	s_mov_b32 s1, s81
	s_mov_b32 s73, s81
	s_mov_b32 s71, s81
	v_writelane_b32 v255, s18, 19
	s_waitcnt vmcnt(0)
	s_branch .LBB0_552

.LBB0_554:
	s_or_b64 exec, exec, s[4:5]
	s_ashr_i32 s95, s94, 31
	s_add_u32 s4, s2, s16
	s_addc_u32 s3, s3, 0
	v_mov_b32_e32 v38, v165
	s_add_u32 s2, s4, 0x2800
	s_addc_u32 s33, s3, 0
	v_readfirstlane_b32 s5, v38
	s_ashr_i32 s79, s5, 6
	v_bfe_u32 v0, v38, 5, 1
	v_and_b32_e32 v175, 31, v38
	s_lshl_b32 s92, s79, 5
	v_lshlrev_b32_e32 v32, 2, v0
	s_add_i32 s82, s92, s78
	v_sub_u32_e32 v1, v175, v32
	v_lshlrev_b32_e32 v176, 4, v0
	s_lshl_b32 s76, s79, 3
	v_bfe_u32 v0, v38, 4, 2
	v_writelane_b32 v255, s16, 17
	v_add_u32_e32 v179, s82, v1
	v_or_b32_e32 v1, s76, v0
	v_and_b32_e32 v2, 15, v38
	s_lshl_b32 s5, s79, 12
	v_and_b32_e32 v39, 63, v38
	v_bitop3_b32 v3, v0, v38, 15 bitop3:0x78
	v_mul_lo_u32 v1, v1, s84
	v_bitop3_b32 v0, v0, v2, 4 bitop3:0x36
	s_add_i32 s93, s5, s77
	s_mul_i32 s5, s79, 0x1c00
	v_readlane_b32 s7, v255, 51
	s_waitcnt vmcnt(16)
	v_lshlrev_b32_e32 v40, 4, v39
	v_lshl_or_b32 v0, v0, 4, v1
	s_lshl_b32 s83, s79, 11
	v_readlane_b32 s6, v255, 53
	s_add_i32 s5, s7, s5
	v_lshl_or_b32 v160, v3, 4, v1
	v_add_u32_e32 v170, 0x1a000, v0
	s_add_i32 s83, s83, s6
	s_add_i32 s98, s79, 2
	s_lshr_b32 s98, s98, 2
	s_lshl_b32 s98, s98, 7
	s_add_i32 s83, s83, s98
	v_add_u32_e32 v180, s5, v40
	s_waitcnt vmcnt(16) lgkmcnt(0)
	ds_write_b128 v180, v[128:131]
	ds_write_b128 v180, v[132:135] offset:1024
	ds_write_b128 v180, v[136:139] offset:2048
	ds_write_b128 v180, v[140:143] offset:3072
	ds_write_b128 v180, v[144:147] offset:4096
	ds_write_b128 v180, v[148:151] offset:5120
	ds_write_b128 v180, v[152:155] offset:6144
	s_add_u32 s4, s4, 0x1a2800
	s_addc_u32 s5, s3, 0
	v_lshl_add_u64 v[0:1], s[4:5], 0, v[160:161]
	s_add_i32 s84, s83, 0x4100
	s_mov_b32 s3, m0
	s_mov_b32 m0, s84
	s_nop 0
	global_load_lds_dwordx4 v[0:1], off
	s_mov_b32 m0, s3
	v_mov_b32_e32 v171, v161
	v_lshl_add_u64 v[0:1], s[4:5], 0, v[170:171]
	s_add_i32 s85, s83, 0x4500
	s_mov_b32 s3, m0
	s_mov_b32 m0, s85
	s_nop 0
	global_load_lds_dwordx4 v[0:1], off
	s_mov_b32 m0, s3
	s_waitcnt lgkmcnt(0)
	s_barrier
	v_lshlrev_b32_e32 v0, 4, v38
	s_movk_i32 s3, 0x70
	v_and_b32_e32 v33, 16, v175
	v_lshlrev_b32_e32 v33, 3, v33
	v_lshl_add_u32 v33, v175, 8, v33
	v_and_b32_e32 v1, 0x70, v0
	v_bitop3_b32 v34, v176, v0, s3 bitop3:0x78
	s_movk_i32 s3, 0x60
	v_add_u32_e32 v2, s6, v33
	v_bitop3_b32 v35, v176, v1, 32 bitop3:0x36
	v_bitop3_b32 v36, v176, v1, 64 bitop3:0x36
	v_bitop3_b32 v37, v176, v1, s3 bitop3:0x36
	v_add_u32_e32 v181, v34, v2
	v_add_u32_e32 v182, v35, v2
	v_add_u32_e32 v183, v36, v2
	v_add_u32_e32 v184, v37, v2
	ds_read_b128 v[0:3], v181 offset:0
	ds_read_b128 v[4:7], v181 offset:0x2080
	ds_read_b128 v[8:11], v180 offset:0
	ds_read_b128 v[42:45], v182 offset:0
	ds_read_b128 v[46:49], v182 offset:0x2080
	ds_read_b128 v[50:53], v180 offset:0x400
	s_waitcnt lgkmcnt(3)
	s_nop 0
	v_mfma_f32_32x32x16_bf16 v[16:31], v[0:3], v[8:11], 0
	v_mfma_f32_32x32x16_bf16 v[0:15], v[4:7], v[8:11], 0
	ds_read_b128 v[54:57], v183 offset:0
	ds_read_b128 v[58:61], v183 offset:0x2080
	ds_read_b128 v[62:65], v180 offset:0x800
	s_waitcnt lgkmcnt(3)
	v_mfma_f32_32x32x16_bf16 v[16:31], v[42:45], v[50:53], v[16:31]
	v_mfma_f32_32x32x16_bf16 v[0:15], v[46:49], v[50:53], v[0:15]
	ds_read_b128 v[42:45], v184 offset:0
	ds_read_b128 v[46:49], v184 offset:0x2080
	ds_read_b128 v[50:53], v180 offset:0xc00
	s_waitcnt lgkmcnt(3)
	v_mfma_f32_32x32x16_bf16 v[16:31], v[54:57], v[62:65], v[16:31]
	v_mfma_f32_32x32x16_bf16 v[0:15], v[58:61], v[62:65], v[0:15]
	ds_read_b128 v[54:57], v181 offset:0x80
	ds_read_b128 v[58:61], v181 offset:0x2100
	ds_read_b128 v[62:65], v180 offset:0x1000
	s_waitcnt lgkmcnt(3)
	v_mfma_f32_32x32x16_bf16 v[16:31], v[42:45], v[50:53], v[16:31]
	v_mfma_f32_32x32x16_bf16 v[0:15], v[46:49], v[50:53], v[0:15]
	ds_read_b128 v[42:45], v182 offset:0x80
	ds_read_b128 v[46:49], v182 offset:0x2100
	ds_read_b128 v[50:53], v180 offset:0x1400
	s_waitcnt lgkmcnt(3)
	v_mfma_f32_32x32x16_bf16 v[16:31], v[54:57], v[62:65], v[16:31]
	v_mfma_f32_32x32x16_bf16 v[0:15], v[58:61], v[62:65], v[0:15]
	ds_read_b128 v[54:57], v183 offset:0x80
	ds_read_b128 v[58:61], v183 offset:0x2100
	ds_read_b128 v[62:65], v180 offset:0x1800
	s_waitcnt lgkmcnt(3)
	v_mfma_f32_32x32x16_bf16 v[16:31], v[42:45], v[50:53], v[16:31]
	v_mfma_f32_32x32x16_bf16 v[0:15], v[46:49], v[50:53], v[0:15]
	ds_read_b128 v[42:45], v184 offset:0x80
	ds_read_b128 v[46:49], v184 offset:0x2100
	s_waitcnt lgkmcnt(2)
	v_mfma_f32_32x32x16_bf16 v[16:31], v[54:57], v[62:65], v[16:31]
	v_mfma_f32_32x32x16_bf16 v[0:15], v[58:61], v[62:65], v[0:15]
	s_waitcnt lgkmcnt(0)
	v_mfma_f32_32x32x16_bf16 v[16:31], v[42:45], v[166:169], v[16:31]
	v_mfma_f32_32x32x16_bf16 v[0:15], v[46:49], v[166:169], v[0:15]
	s_bitcmp0_b32 s100, 8
	s_cbranch_scc1 .Lstg_a9
	s_waitcnt vmcnt(0)
	s_waitcnt lgkmcnt(0)
	s_barrier

.LBB0_557:
	ds_read_b64_tr_b16 v[144:145], v177 offset:0
	ds_read_b64_tr_b16 v[146:147], v177 offset:0x1000
	ds_read_b64_tr_b16 v[148:149], v177 offset:0x2000
	ds_read_b64_tr_b16 v[150:151], v177 offset:0x3000
	ds_read_b64_tr_b16 v[152:153], v177 offset:0x4000
	ds_read_b64_tr_b16 v[154:155], v177 offset:0x5000
	ds_read_b64_tr_b16 v[156:157], v177 offset:0x6000
	ds_read_b64_tr_b16 v[158:159], v177 offset:0x7000
	ds_read_b64_tr_b16 v[192:193], v177 offset:0x200
	ds_read_b64_tr_b16 v[194:195], v177 offset:0x1200
	ds_read_b64_tr_b16 v[196:197], v177 offset:0x2200
	ds_read_b64_tr_b16 v[198:199], v177 offset:0x3200
	ds_read_b64_tr_b16 v[200:201], v177 offset:0x4200
	ds_read_b64_tr_b16 v[202:203], v177 offset:0x5200
	ds_read_b64_tr_b16 v[204:205], v177 offset:0x6200
	ds_read_b64_tr_b16 v[206:207], v177 offset:0x7200
	s_waitcnt lgkmcnt(8)
	s_nop 0
	v_mfma_f32_32x32x16_bf16 v[112:127], v[144:147], v[128:131], v[112:127]
	v_mfma_f32_32x32x16_bf16 v[112:127], v[148:151], v[132:135], v[112:127]
	v_mfma_f32_32x32x16_bf16 v[112:127], v[152:155], v[136:139], v[112:127]
	v_mfma_f32_32x32x16_bf16 v[112:127], v[156:159], v[140:143], v[112:127]
	ds_read_b64_tr_b16 v[144:145], v177 offset:0x400
	ds_read_b64_tr_b16 v[146:147], v177 offset:0x1400
	ds_read_b64_tr_b16 v[148:149], v177 offset:0x2400
	ds_read_b64_tr_b16 v[150:151], v177 offset:0x3400
	ds_read_b64_tr_b16 v[152:153], v177 offset:0x4400
	ds_read_b64_tr_b16 v[154:155], v177 offset:0x5400
	ds_read_b64_tr_b16 v[156:157], v177 offset:0x6400
	ds_read_b64_tr_b16 v[158:159], v177 offset:0x7400
	s_waitcnt lgkmcnt(8)
	v_mfma_f32_32x32x16_bf16 v[80:95], v[192:195], v[128:131], v[80:95]
	v_mfma_f32_32x32x16_bf16 v[80:95], v[196:199], v[132:135], v[80:95]
	v_mfma_f32_32x32x16_bf16 v[80:95], v[200:203], v[136:139], v[80:95]
	v_mfma_f32_32x32x16_bf16 v[80:95], v[204:207], v[140:143], v[80:95]
	ds_read_b64_tr_b16 v[192:193], v177 offset:0x600
	ds_read_b64_tr_b16 v[194:195], v177 offset:0x1600
	ds_read_b64_tr_b16 v[196:197], v177 offset:0x2600
	ds_read_b64_tr_b16 v[198:199], v177 offset:0x3600
	ds_read_b64_tr_b16 v[200:201], v177 offset:0x4600
	ds_read_b64_tr_b16 v[202:203], v177 offset:0x5600
	ds_read_b64_tr_b16 v[204:205], v177 offset:0x6600
	ds_read_b64_tr_b16 v[206:207], v177 offset:0x7600
	s_waitcnt lgkmcnt(8)
	v_mfma_f32_32x32x16_bf16 v[96:111], v[144:147], v[128:131], v[96:111]
	v_mfma_f32_32x32x16_bf16 v[96:111], v[148:151], v[132:135], v[96:111]
	v_mfma_f32_32x32x16_bf16 v[96:111], v[152:155], v[136:139], v[96:111]
	v_mfma_f32_32x32x16_bf16 v[96:111], v[156:159], v[140:143], v[96:111]
	ds_read_b64_tr_b16 v[144:145], v177 offset:0x800
	ds_read_b64_tr_b16 v[146:147], v177 offset:0x1800
	ds_read_b64_tr_b16 v[148:149], v177 offset:0x2800
	ds_read_b64_tr_b16 v[150:151], v177 offset:0x3800
	ds_read_b64_tr_b16 v[152:153], v177 offset:0x4800
	ds_read_b64_tr_b16 v[154:155], v177 offset:0x5800
	ds_read_b64_tr_b16 v[156:157], v177 offset:0x6800
	ds_read_b64_tr_b16 v[158:159], v177 offset:0x7800
	s_waitcnt lgkmcnt(8)
	v_mfma_f32_32x32x16_bf16 v[64:79], v[192:195], v[128:131], v[64:79]
	v_mfma_f32_32x32x16_bf16 v[64:79], v[196:199], v[132:135], v[64:79]
	v_mfma_f32_32x32x16_bf16 v[64:79], v[200:203], v[136:139], v[64:79]
	v_mfma_f32_32x32x16_bf16 v[64:79], v[204:207], v[140:143], v[64:79]
	ds_read_b64_tr_b16 v[192:193], v177 offset:0xa00
	ds_read_b64_tr_b16 v[194:195], v177 offset:0x1a00
	ds_read_b64_tr_b16 v[196:197], v177 offset:0x2a00
	ds_read_b64_tr_b16 v[198:199], v177 offset:0x3a00
	ds_read_b64_tr_b16 v[200:201], v177 offset:0x4a00
	ds_read_b64_tr_b16 v[202:203], v177 offset:0x5a00
	ds_read_b64_tr_b16 v[204:205], v177 offset:0x6a00
	ds_read_b64_tr_b16 v[206:207], v177 offset:0x7a00
	s_waitcnt lgkmcnt(8)
	v_mfma_f32_32x32x16_bf16 v[48:63], v[144:147], v[128:131], v[48:63]
	v_mfma_f32_32x32x16_bf16 v[48:63], v[148:151], v[132:135], v[48:63]
	v_mfma_f32_32x32x16_bf16 v[48:63], v[152:155], v[136:139], v[48:63]
	v_mfma_f32_32x32x16_bf16 v[48:63], v[156:159], v[140:143], v[48:63]
	ds_read_b64_tr_b16 v[144:145], v177 offset:0xc00
	ds_read_b64_tr_b16 v[146:147], v177 offset:0x1c00
	ds_read_b64_tr_b16 v[148:149], v177 offset:0x2c00
	ds_read_b64_tr_b16 v[150:151], v177 offset:0x3c00
	ds_read_b64_tr_b16 v[152:153], v177 offset:0x4c00
	ds_read_b64_tr_b16 v[154:155], v177 offset:0x5c00
	ds_read_b64_tr_b16 v[156:157], v177 offset:0x6c00
	ds_read_b64_tr_b16 v[158:159], v177 offset:0x7c00
	s_waitcnt lgkmcnt(8)
	v_mfma_f32_32x32x16_bf16 v[32:47], v[192:195], v[128:131], v[32:47]
	v_mfma_f32_32x32x16_bf16 v[32:47], v[196:199], v[132:135], v[32:47]
	v_mfma_f32_32x32x16_bf16 v[32:47], v[200:203], v[136:139], v[32:47]
	v_mfma_f32_32x32x16_bf16 v[32:47], v[204:207], v[140:143], v[32:47]
	ds_read_b64_tr_b16 v[192:193], v177 offset:0xe00
	ds_read_b64_tr_b16 v[194:195], v177 offset:0x1e00
	ds_read_b64_tr_b16 v[196:197], v177 offset:0x2e00
	ds_read_b64_tr_b16 v[198:199], v177 offset:0x3e00
	ds_read_b64_tr_b16 v[200:201], v177 offset:0x4e00
	ds_read_b64_tr_b16 v[202:203], v177 offset:0x5e00
	ds_read_b64_tr_b16 v[204:205], v177 offset:0x6e00
	ds_read_b64_tr_b16 v[206:207], v177 offset:0x7e00
	s_waitcnt lgkmcnt(8)
	v_mfma_f32_32x32x16_bf16 v[16:31], v[144:147], v[128:131], v[16:31]
	v_mfma_f32_32x32x16_bf16 v[16:31], v[148:151], v[132:135], v[16:31]
	v_mfma_f32_32x32x16_bf16 v[16:31], v[152:155], v[136:139], v[16:31]
	v_mfma_f32_32x32x16_bf16 v[16:31], v[156:159], v[140:143], v[16:31]
	s_waitcnt lgkmcnt(0)
	v_mfma_f32_32x32x16_bf16 v[0:15], v[192:195], v[128:131], v[0:15]
	v_mfma_f32_32x32x16_bf16 v[0:15], v[196:199], v[132:135], v[0:15]
	v_mfma_f32_32x32x16_bf16 v[0:15], v[200:203], v[136:139], v[0:15]
	v_mfma_f32_32x32x16_bf16 v[0:15], v[204:207], v[140:143], v[0:15]
	ds_read_b128 v[128:131], v188 offset:0
	ds_read_b128 v[132:135], v188 offset:0x2080
	ds_read_b128 v[136:139], v180 offset:0
	ds_read_b128 v[192:195], v187 offset:0
	ds_read_b128 v[196:199], v187 offset:0x2080
	ds_read_b128 v[200:203], v180 offset:0x400
	s_waitcnt lgkmcnt(3)
	s_nop 0
	v_mfma_f32_32x32x16_bf16 v[144:159], v[128:131], v[136:139], 0
	v_mfma_f32_32x32x16_bf16 v[128:143], v[132:135], v[136:139], 0
	ds_read_b128 v[204:207], v186 offset:0
	ds_read_b128 v[208:211], v186 offset:0x2080
	ds_read_b128 v[212:215], v180 offset:0x800
	s_waitcnt lgkmcnt(3)
	v_mfma_f32_32x32x16_bf16 v[144:159], v[192:195], v[200:203], v[144:159]
	v_mfma_f32_32x32x16_bf16 v[128:143], v[196:199], v[200:203], v[128:143]
	ds_read_b128 v[192:195], v185 offset:0
	ds_read_b128 v[196:199], v185 offset:0x2080
	ds_read_b128 v[200:203], v180 offset:0xc00
	s_waitcnt lgkmcnt(3)
	v_mfma_f32_32x32x16_bf16 v[144:159], v[204:207], v[212:215], v[144:159]
	v_mfma_f32_32x32x16_bf16 v[128:143], v[208:211], v[212:215], v[128:143]
	ds_read_b128 v[204:207], v188 offset:0x80
	ds_read_b128 v[208:211], v188 offset:0x2100
	ds_read_b128 v[212:215], v180 offset:0x1000
	s_waitcnt lgkmcnt(3)
	v_mfma_f32_32x32x16_bf16 v[144:159], v[192:195], v[200:203], v[144:159]
	v_mfma_f32_32x32x16_bf16 v[128:143], v[196:199], v[200:203], v[128:143]
	ds_read_b128 v[192:195], v187 offset:0x80
	ds_read_b128 v[196:199], v187 offset:0x2100
	ds_read_b128 v[200:203], v180 offset:0x1400
	s_waitcnt lgkmcnt(3)
	v_mfma_f32_32x32x16_bf16 v[144:159], v[204:207], v[212:215], v[144:159]
	v_mfma_f32_32x32x16_bf16 v[128:143], v[208:211], v[212:215], v[128:143]
	ds_read_b128 v[204:207], v186 offset:0x80
	ds_read_b128 v[208:211], v186 offset:0x2100
	ds_read_b128 v[212:215], v180 offset:0x1800
	s_waitcnt lgkmcnt(3)
	v_mfma_f32_32x32x16_bf16 v[144:159], v[192:195], v[200:203], v[144:159]
	v_mfma_f32_32x32x16_bf16 v[128:143], v[196:199], v[200:203], v[128:143]
	ds_read_b128 v[192:195], v185 offset:0x80
	ds_read_b128 v[196:199], v185 offset:0x2100
	s_waitcnt lgkmcnt(2)
	v_mfma_f32_32x32x16_bf16 v[144:159], v[204:207], v[212:215], v[144:159]
	v_mfma_f32_32x32x16_bf16 v[128:143], v[208:211], v[212:215], v[128:143]
	s_waitcnt lgkmcnt(0)
	v_mfma_f32_32x32x16_bf16 v[144:159], v[192:195], v[166:169], v[144:159]
	v_mfma_f32_32x32x16_bf16 v[128:143], v[196:199], v[166:169], v[128:143]
	s_bitcmp0_b32 s100, 8
	s_cbranch_scc1 .Lstg_a10
	s_waitcnt vmcnt(0)
	s_waitcnt lgkmcnt(0)
	s_barrier

.LBB0_565:
	ds_read_b64_tr_b16 v[144:145], v177 offset:0x8000
	ds_read_b64_tr_b16 v[146:147], v177 offset:0x9000
	ds_read_b64_tr_b16 v[148:149], v177 offset:0xa000
	ds_read_b64_tr_b16 v[150:151], v177 offset:0xb000
	ds_read_b64_tr_b16 v[152:153], v177 offset:0xc000
	ds_read_b64_tr_b16 v[154:155], v177 offset:0xd000
	ds_read_b64_tr_b16 v[156:157], v177 offset:0xe000
	ds_read_b64_tr_b16 v[158:159], v177 offset:0xf000
	ds_read_b64_tr_b16 v[194:195], v177 offset:0x8200
	ds_read_b64_tr_b16 v[196:197], v177 offset:0x9200
	ds_read_b64_tr_b16 v[198:199], v177 offset:0xa200
	ds_read_b64_tr_b16 v[200:201], v177 offset:0xb200
	ds_read_b64_tr_b16 v[202:203], v177 offset:0xc200
	ds_read_b64_tr_b16 v[204:205], v177 offset:0xd200
	ds_read_b64_tr_b16 v[206:207], v177 offset:0xe200
	ds_read_b64_tr_b16 v[208:209], v177 offset:0xf200
	s_waitcnt lgkmcnt(8)
	s_nop 0
	v_mfma_f32_32x32x16_bf16 v[112:127], v[144:147], v[128:131], v[112:127]
	v_mfma_f32_32x32x16_bf16 v[112:127], v[148:151], v[132:135], v[112:127]
	v_mfma_f32_32x32x16_bf16 v[112:127], v[152:155], v[136:139], v[112:127]
	v_mfma_f32_32x32x16_bf16 v[112:127], v[156:159], v[140:143], v[112:127]
	ds_read_b64_tr_b16 v[144:145], v177 offset:0x8400
	ds_read_b64_tr_b16 v[146:147], v177 offset:0x9400
	ds_read_b64_tr_b16 v[148:149], v177 offset:0xa400
	ds_read_b64_tr_b16 v[150:151], v177 offset:0xb400
	ds_read_b64_tr_b16 v[152:153], v177 offset:0xc400
	ds_read_b64_tr_b16 v[154:155], v177 offset:0xd400
	ds_read_b64_tr_b16 v[156:157], v177 offset:0xe400
	ds_read_b64_tr_b16 v[158:159], v177 offset:0xf400
	s_waitcnt lgkmcnt(8)
	v_mfma_f32_32x32x16_bf16 v[80:95], v[194:197], v[128:131], v[80:95]
	v_mfma_f32_32x32x16_bf16 v[80:95], v[198:201], v[132:135], v[80:95]
	v_mfma_f32_32x32x16_bf16 v[80:95], v[202:205], v[136:139], v[80:95]
	v_mfma_f32_32x32x16_bf16 v[80:95], v[206:209], v[140:143], v[80:95]
	ds_read_b64_tr_b16 v[194:195], v177 offset:0x8600
	ds_read_b64_tr_b16 v[196:197], v177 offset:0x9600
	ds_read_b64_tr_b16 v[198:199], v177 offset:0xa600
	ds_read_b64_tr_b16 v[200:201], v177 offset:0xb600
	ds_read_b64_tr_b16 v[202:203], v177 offset:0xc600
	ds_read_b64_tr_b16 v[204:205], v177 offset:0xd600
	ds_read_b64_tr_b16 v[206:207], v177 offset:0xe600
	ds_read_b64_tr_b16 v[208:209], v177 offset:0xf600
	s_waitcnt lgkmcnt(8)
	v_mfma_f32_32x32x16_bf16 v[96:111], v[144:147], v[128:131], v[96:111]
	v_mfma_f32_32x32x16_bf16 v[96:111], v[148:151], v[132:135], v[96:111]
	v_mfma_f32_32x32x16_bf16 v[96:111], v[152:155], v[136:139], v[96:111]
	v_mfma_f32_32x32x16_bf16 v[96:111], v[156:159], v[140:143], v[96:111]
	ds_read_b64_tr_b16 v[144:145], v177 offset:0x8800
	ds_read_b64_tr_b16 v[146:147], v177 offset:0x9800
	ds_read_b64_tr_b16 v[148:149], v177 offset:0xa800
	ds_read_b64_tr_b16 v[150:151], v177 offset:0xb800
	ds_read_b64_tr_b16 v[152:153], v177 offset:0xc800
	ds_read_b64_tr_b16 v[154:155], v177 offset:0xd800
	ds_read_b64_tr_b16 v[156:157], v177 offset:0xe800
	ds_read_b64_tr_b16 v[158:159], v177 offset:0xf800
	s_waitcnt lgkmcnt(8)
	v_mfma_f32_32x32x16_bf16 v[64:79], v[194:197], v[128:131], v[64:79]
	v_mfma_f32_32x32x16_bf16 v[64:79], v[198:201], v[132:135], v[64:79]
	v_mfma_f32_32x32x16_bf16 v[64:79], v[202:205], v[136:139], v[64:79]
	v_mfma_f32_32x32x16_bf16 v[64:79], v[206:209], v[140:143], v[64:79]
	ds_read_b64_tr_b16 v[194:195], v177 offset:0x8a00
	ds_read_b64_tr_b16 v[196:197], v177 offset:0x9a00
	ds_read_b64_tr_b16 v[198:199], v177 offset:0xaa00
	ds_read_b64_tr_b16 v[200:201], v177 offset:0xba00
	ds_read_b64_tr_b16 v[202:203], v177 offset:0xca00
	ds_read_b64_tr_b16 v[204:205], v177 offset:0xda00
	ds_read_b64_tr_b16 v[206:207], v177 offset:0xea00
	ds_read_b64_tr_b16 v[208:209], v177 offset:0xfa00
	s_waitcnt lgkmcnt(8)
	v_mfma_f32_32x32x16_bf16 v[48:63], v[144:147], v[128:131], v[48:63]
	v_mfma_f32_32x32x16_bf16 v[48:63], v[148:151], v[132:135], v[48:63]
	v_mfma_f32_32x32x16_bf16 v[48:63], v[152:155], v[136:139], v[48:63]
	v_mfma_f32_32x32x16_bf16 v[48:63], v[156:159], v[140:143], v[48:63]
	ds_read_b64_tr_b16 v[144:145], v177 offset:0x8c00
	ds_read_b64_tr_b16 v[146:147], v177 offset:0x9c00
	ds_read_b64_tr_b16 v[148:149], v177 offset:0xac00
	ds_read_b64_tr_b16 v[150:151], v177 offset:0xbc00
	ds_read_b64_tr_b16 v[152:153], v177 offset:0xcc00
	ds_read_b64_tr_b16 v[154:155], v177 offset:0xdc00
	ds_read_b64_tr_b16 v[156:157], v177 offset:0xec00
	ds_read_b64_tr_b16 v[158:159], v177 offset:0xfc00
	s_waitcnt lgkmcnt(8)
	v_mfma_f32_32x32x16_bf16 v[32:47], v[194:197], v[128:131], v[32:47]
	v_mfma_f32_32x32x16_bf16 v[32:47], v[198:201], v[132:135], v[32:47]
	v_mfma_f32_32x32x16_bf16 v[32:47], v[202:205], v[136:139], v[32:47]
	v_mfma_f32_32x32x16_bf16 v[32:47], v[206:209], v[140:143], v[32:47]
	ds_read_b64_tr_b16 v[194:195], v177 offset:0x8e00
	ds_read_b64_tr_b16 v[196:197], v177 offset:0x9e00
	ds_read_b64_tr_b16 v[198:199], v177 offset:0xae00
	ds_read_b64_tr_b16 v[200:201], v177 offset:0xbe00
	ds_read_b64_tr_b16 v[202:203], v177 offset:0xce00
	ds_read_b64_tr_b16 v[204:205], v177 offset:0xde00
	ds_read_b64_tr_b16 v[206:207], v177 offset:0xee00
	ds_read_b64_tr_b16 v[208:209], v177 offset:0xfe00
	s_waitcnt lgkmcnt(8)
	v_mfma_f32_32x32x16_bf16 v[16:31], v[144:147], v[128:131], v[16:31]
	v_mfma_f32_32x32x16_bf16 v[16:31], v[148:151], v[132:135], v[16:31]
	v_mfma_f32_32x32x16_bf16 v[16:31], v[152:155], v[136:139], v[16:31]
	v_mfma_f32_32x32x16_bf16 v[16:31], v[156:159], v[140:143], v[16:31]
	s_waitcnt lgkmcnt(0)
	v_mfma_f32_32x32x16_bf16 v[0:15], v[194:197], v[128:131], v[0:15]
	v_mfma_f32_32x32x16_bf16 v[0:15], v[198:201], v[132:135], v[0:15]
	v_mfma_f32_32x32x16_bf16 v[0:15], v[202:205], v[136:139], v[0:15]
	v_mfma_f32_32x32x16_bf16 v[0:15], v[206:209], v[140:143], v[0:15]
	ds_read_b128 v[128:131], v181 offset:0
	ds_read_b128 v[132:135], v181 offset:0x2080
	ds_read_b128 v[136:139], v180 offset:0
	ds_read_b128 v[194:197], v182 offset:0
	ds_read_b128 v[198:201], v182 offset:0x2080
	ds_read_b128 v[202:205], v180 offset:0x400
	s_waitcnt lgkmcnt(3)
	s_nop 0
	v_mfma_f32_32x32x16_bf16 v[144:159], v[128:131], v[136:139], 0
	v_mfma_f32_32x32x16_bf16 v[128:143], v[132:135], v[136:139], 0
	ds_read_b128 v[206:209], v183 offset:0
	ds_read_b128 v[210:213], v183 offset:0x2080
	ds_read_b128 v[214:217], v180 offset:0x800
	s_waitcnt lgkmcnt(3)
	v_mfma_f32_32x32x16_bf16 v[144:159], v[194:197], v[202:205], v[144:159]
	v_mfma_f32_32x32x16_bf16 v[128:143], v[198:201], v[202:205], v[128:143]
	ds_read_b128 v[194:197], v184 offset:0
	ds_read_b128 v[198:201], v184 offset:0x2080
	ds_read_b128 v[202:205], v180 offset:0xc00
	s_waitcnt lgkmcnt(3)
	v_mfma_f32_32x32x16_bf16 v[144:159], v[206:209], v[214:217], v[144:159]
	v_mfma_f32_32x32x16_bf16 v[128:143], v[210:213], v[214:217], v[128:143]
	ds_read_b128 v[206:209], v181 offset:0x80
	ds_read_b128 v[210:213], v181 offset:0x2100
	ds_read_b128 v[214:217], v180 offset:0x1000
	s_waitcnt lgkmcnt(3)
	v_mfma_f32_32x32x16_bf16 v[144:159], v[194:197], v[202:205], v[144:159]
	v_mfma_f32_32x32x16_bf16 v[128:143], v[198:201], v[202:205], v[128:143]
	ds_read_b128 v[194:197], v182 offset:0x80
	ds_read_b128 v[198:201], v182 offset:0x2100
	ds_read_b128 v[202:205], v180 offset:0x1400
	s_waitcnt lgkmcnt(3)
	v_mfma_f32_32x32x16_bf16 v[144:159], v[206:209], v[214:217], v[144:159]
	v_mfma_f32_32x32x16_bf16 v[128:143], v[210:213], v[214:217], v[128:143]
	ds_read_b128 v[206:209], v183 offset:0x80
	ds_read_b128 v[210:213], v183 offset:0x2100
	ds_read_b128 v[214:217], v180 offset:0x1800
	s_waitcnt lgkmcnt(3)
	v_mfma_f32_32x32x16_bf16 v[144:159], v[194:197], v[202:205], v[144:159]
	v_mfma_f32_32x32x16_bf16 v[128:143], v[198:201], v[202:205], v[128:143]
	ds_read_b128 v[194:197], v184 offset:0x80
	ds_read_b128 v[198:201], v184 offset:0x2100
	s_waitcnt lgkmcnt(2)
	v_mfma_f32_32x32x16_bf16 v[144:159], v[206:209], v[214:217], v[144:159]
	v_mfma_f32_32x32x16_bf16 v[128:143], v[210:213], v[214:217], v[128:143]
	s_waitcnt lgkmcnt(0)
	v_mfma_f32_32x32x16_bf16 v[144:159], v[194:197], v[166:169], v[144:159]
	v_mfma_f32_32x32x16_bf16 v[128:143], v[198:201], v[166:169], v[128:143]
	s_bitcmp0_b32 s100, 8
	s_cbranch_scc1 .Lstg_a11
	s_waitcnt vmcnt(0)
	s_waitcnt lgkmcnt(0)
	s_barrier

.LBB0_580:
	ds_read_b64_tr_b16 v[144:145], v177 offset:0
	ds_read_b64_tr_b16 v[146:147], v177 offset:0x1000
	ds_read_b64_tr_b16 v[148:149], v177 offset:0x2000
	ds_read_b64_tr_b16 v[150:151], v177 offset:0x3000
	ds_read_b64_tr_b16 v[152:153], v177 offset:0x4000
	ds_read_b64_tr_b16 v[154:155], v177 offset:0x5000
	ds_read_b64_tr_b16 v[156:157], v177 offset:0x6000
	ds_read_b64_tr_b16 v[158:159], v177 offset:0x7000
	ds_read_b64_tr_b16 v[192:193], v177 offset:0x200
	ds_read_b64_tr_b16 v[194:195], v177 offset:0x1200
	ds_read_b64_tr_b16 v[196:197], v177 offset:0x2200
	ds_read_b64_tr_b16 v[198:199], v177 offset:0x3200
	ds_read_b64_tr_b16 v[200:201], v177 offset:0x4200
	ds_read_b64_tr_b16 v[202:203], v177 offset:0x5200
	ds_read_b64_tr_b16 v[204:205], v177 offset:0x6200
	ds_read_b64_tr_b16 v[206:207], v177 offset:0x7200
	s_waitcnt lgkmcnt(8)
	s_nop 0
	v_mfma_f32_32x32x16_bf16 v[112:127], v[144:147], v[128:131], v[112:127]
	v_mfma_f32_32x32x16_bf16 v[112:127], v[148:151], v[132:135], v[112:127]
	v_mfma_f32_32x32x16_bf16 v[112:127], v[152:155], v[136:139], v[112:127]
	v_mfma_f32_32x32x16_bf16 v[112:127], v[156:159], v[140:143], v[112:127]
	ds_read_b64_tr_b16 v[144:145], v177 offset:0x400
	ds_read_b64_tr_b16 v[146:147], v177 offset:0x1400
	ds_read_b64_tr_b16 v[148:149], v177 offset:0x2400
	ds_read_b64_tr_b16 v[150:151], v177 offset:0x3400
	ds_read_b64_tr_b16 v[152:153], v177 offset:0x4400
	ds_read_b64_tr_b16 v[154:155], v177 offset:0x5400
	ds_read_b64_tr_b16 v[156:157], v177 offset:0x6400
	ds_read_b64_tr_b16 v[158:159], v177 offset:0x7400
	s_waitcnt lgkmcnt(8)
	v_mfma_f32_32x32x16_bf16 v[80:95], v[192:195], v[128:131], v[80:95]
	v_mfma_f32_32x32x16_bf16 v[80:95], v[196:199], v[132:135], v[80:95]
	v_mfma_f32_32x32x16_bf16 v[80:95], v[200:203], v[136:139], v[80:95]
	v_mfma_f32_32x32x16_bf16 v[80:95], v[204:207], v[140:143], v[80:95]
	ds_read_b64_tr_b16 v[192:193], v177 offset:0x600
	ds_read_b64_tr_b16 v[194:195], v177 offset:0x1600
	ds_read_b64_tr_b16 v[196:197], v177 offset:0x2600
	ds_read_b64_tr_b16 v[198:199], v177 offset:0x3600
	ds_read_b64_tr_b16 v[200:201], v177 offset:0x4600
	ds_read_b64_tr_b16 v[202:203], v177 offset:0x5600
	ds_read_b64_tr_b16 v[204:205], v177 offset:0x6600
	ds_read_b64_tr_b16 v[206:207], v177 offset:0x7600
	s_waitcnt lgkmcnt(8)
	v_mfma_f32_32x32x16_bf16 v[96:111], v[144:147], v[128:131], v[96:111]
	v_mfma_f32_32x32x16_bf16 v[96:111], v[148:151], v[132:135], v[96:111]
	v_mfma_f32_32x32x16_bf16 v[96:111], v[152:155], v[136:139], v[96:111]
	v_mfma_f32_32x32x16_bf16 v[96:111], v[156:159], v[140:143], v[96:111]
	ds_read_b64_tr_b16 v[144:145], v177 offset:0x800
	ds_read_b64_tr_b16 v[146:147], v177 offset:0x1800
	ds_read_b64_tr_b16 v[148:149], v177 offset:0x2800
	ds_read_b64_tr_b16 v[150:151], v177 offset:0x3800
	ds_read_b64_tr_b16 v[152:153], v177 offset:0x4800
	ds_read_b64_tr_b16 v[154:155], v177 offset:0x5800
	ds_read_b64_tr_b16 v[156:157], v177 offset:0x6800
	ds_read_b64_tr_b16 v[158:159], v177 offset:0x7800
	s_waitcnt lgkmcnt(8)
	v_mfma_f32_32x32x16_bf16 v[64:79], v[192:195], v[128:131], v[64:79]
	v_mfma_f32_32x32x16_bf16 v[64:79], v[196:199], v[132:135], v[64:79]
	v_mfma_f32_32x32x16_bf16 v[64:79], v[200:203], v[136:139], v[64:79]
	v_mfma_f32_32x32x16_bf16 v[64:79], v[204:207], v[140:143], v[64:79]
	ds_read_b64_tr_b16 v[192:193], v177 offset:0xa00
	ds_read_b64_tr_b16 v[194:195], v177 offset:0x1a00
	ds_read_b64_tr_b16 v[196:197], v177 offset:0x2a00
	ds_read_b64_tr_b16 v[198:199], v177 offset:0x3a00
	ds_read_b64_tr_b16 v[200:201], v177 offset:0x4a00
	ds_read_b64_tr_b16 v[202:203], v177 offset:0x5a00
	ds_read_b64_tr_b16 v[204:205], v177 offset:0x6a00
	ds_read_b64_tr_b16 v[206:207], v177 offset:0x7a00
	s_waitcnt lgkmcnt(8)
	v_mfma_f32_32x32x16_bf16 v[48:63], v[144:147], v[128:131], v[48:63]
	v_mfma_f32_32x32x16_bf16 v[48:63], v[148:151], v[132:135], v[48:63]
	v_mfma_f32_32x32x16_bf16 v[48:63], v[152:155], v[136:139], v[48:63]
	v_mfma_f32_32x32x16_bf16 v[48:63], v[156:159], v[140:143], v[48:63]
	ds_read_b64_tr_b16 v[144:145], v177 offset:0xc00
	ds_read_b64_tr_b16 v[146:147], v177 offset:0x1c00
	ds_read_b64_tr_b16 v[148:149], v177 offset:0x2c00
	ds_read_b64_tr_b16 v[150:151], v177 offset:0x3c00
	ds_read_b64_tr_b16 v[152:153], v177 offset:0x4c00
	ds_read_b64_tr_b16 v[154:155], v177 offset:0x5c00
	ds_read_b64_tr_b16 v[156:157], v177 offset:0x6c00
	ds_read_b64_tr_b16 v[158:159], v177 offset:0x7c00
	s_waitcnt lgkmcnt(8)
	v_mfma_f32_32x32x16_bf16 v[32:47], v[192:195], v[128:131], v[32:47]
	v_mfma_f32_32x32x16_bf16 v[32:47], v[196:199], v[132:135], v[32:47]
	v_mfma_f32_32x32x16_bf16 v[32:47], v[200:203], v[136:139], v[32:47]
	v_mfma_f32_32x32x16_bf16 v[32:47], v[204:207], v[140:143], v[32:47]
	ds_read_b64_tr_b16 v[192:193], v177 offset:0xe00
	ds_read_b64_tr_b16 v[194:195], v177 offset:0x1e00
	ds_read_b64_tr_b16 v[196:197], v177 offset:0x2e00
	ds_read_b64_tr_b16 v[198:199], v177 offset:0x3e00
	ds_read_b64_tr_b16 v[200:201], v177 offset:0x4e00
	ds_read_b64_tr_b16 v[202:203], v177 offset:0x5e00
	ds_read_b64_tr_b16 v[204:205], v177 offset:0x6e00
	ds_read_b64_tr_b16 v[206:207], v177 offset:0x7e00
	s_waitcnt lgkmcnt(8)
	v_mfma_f32_32x32x16_bf16 v[16:31], v[144:147], v[128:131], v[16:31]
	v_mfma_f32_32x32x16_bf16 v[16:31], v[148:151], v[132:135], v[16:31]
	v_mfma_f32_32x32x16_bf16 v[16:31], v[152:155], v[136:139], v[16:31]
	v_mfma_f32_32x32x16_bf16 v[16:31], v[156:159], v[140:143], v[16:31]
	s_waitcnt lgkmcnt(0)
	v_mfma_f32_32x32x16_bf16 v[0:15], v[192:195], v[128:131], v[0:15]
	v_mfma_f32_32x32x16_bf16 v[0:15], v[196:199], v[132:135], v[0:15]
	v_mfma_f32_32x32x16_bf16 v[0:15], v[200:203], v[136:139], v[0:15]
	v_mfma_f32_32x32x16_bf16 v[0:15], v[204:207], v[140:143], v[0:15]
	ds_read_b128 v[128:131], v188 offset:0
	ds_read_b128 v[132:135], v188 offset:0x2080
	ds_read_b128 v[136:139], v180 offset:0
	ds_read_b128 v[192:195], v187 offset:0
	ds_read_b128 v[196:199], v187 offset:0x2080
	ds_read_b128 v[200:203], v180 offset:0x400
	s_waitcnt lgkmcnt(3)
	s_nop 0
	v_mfma_f32_32x32x16_bf16 v[144:159], v[128:131], v[136:139], 0
	v_mfma_f32_32x32x16_bf16 v[128:143], v[132:135], v[136:139], 0
	ds_read_b128 v[204:207], v186 offset:0
	ds_read_b128 v[208:211], v186 offset:0x2080
	ds_read_b128 v[212:215], v180 offset:0x800
	s_waitcnt lgkmcnt(3)
	v_mfma_f32_32x32x16_bf16 v[144:159], v[192:195], v[200:203], v[144:159]
	v_mfma_f32_32x32x16_bf16 v[128:143], v[196:199], v[200:203], v[128:143]
	ds_read_b128 v[192:195], v185 offset:0
	ds_read_b128 v[196:199], v185 offset:0x2080
	ds_read_b128 v[200:203], v180 offset:0xc00
	s_waitcnt lgkmcnt(3)
	v_mfma_f32_32x32x16_bf16 v[144:159], v[204:207], v[212:215], v[144:159]
	v_mfma_f32_32x32x16_bf16 v[128:143], v[208:211], v[212:215], v[128:143]
	ds_read_b128 v[204:207], v188 offset:0x80
	ds_read_b128 v[208:211], v188 offset:0x2100
	ds_read_b128 v[212:215], v180 offset:0x1000
	s_waitcnt lgkmcnt(3)
	v_mfma_f32_32x32x16_bf16 v[144:159], v[192:195], v[200:203], v[144:159]
	v_mfma_f32_32x32x16_bf16 v[128:143], v[196:199], v[200:203], v[128:143]
	ds_read_b128 v[192:195], v187 offset:0x80
	ds_read_b128 v[196:199], v187 offset:0x2100
	ds_read_b128 v[200:203], v180 offset:0x1400
	s_waitcnt lgkmcnt(3)
	v_mfma_f32_32x32x16_bf16 v[144:159], v[204:207], v[212:215], v[144:159]
	v_mfma_f32_32x32x16_bf16 v[128:143], v[208:211], v[212:215], v[128:143]
	ds_read_b128 v[204:207], v186 offset:0x80
	ds_read_b128 v[208:211], v186 offset:0x2100
	ds_read_b128 v[186:189], v180 offset:0x1800
	s_waitcnt lgkmcnt(3)
	v_mfma_f32_32x32x16_bf16 v[144:159], v[192:195], v[200:203], v[144:159]
	v_mfma_f32_32x32x16_bf16 v[128:143], v[196:199], v[200:203], v[128:143]
	ds_read_b128 v[180:183], v185 offset:0x80
	ds_read_b128 v[192:195], v185 offset:0x2100
	s_waitcnt lgkmcnt(2)
	v_mfma_f32_32x32x16_bf16 v[144:159], v[204:207], v[186:189], v[144:159]
	v_mfma_f32_32x32x16_bf16 v[128:143], v[208:211], v[186:189], v[128:143]
	s_waitcnt lgkmcnt(0)
	v_mfma_f32_32x32x16_bf16 v[144:159], v[180:183], v[166:169], v[144:159]
	v_mfma_f32_32x32x16_bf16 v[128:143], v[192:195], v[166:169], v[128:143]
	s_bitcmp0_b32 s100, 8
	s_cbranch_scc1 .Lstg_a12
	s_waitcnt vmcnt(0)
	s_waitcnt lgkmcnt(0)
	s_barrier

.LBB0_586:
	s_or_b64 exec, exec, s[4:5]
	v_mov_b32_e32 v38, v165
	v_readlane_b32 s5, v255, 51
	v_readfirstlane_b32 s2, v38
	s_ashr_i32 s79, s2, 6
	v_bfe_u32 v0, v38, 5, 1
	v_and_b32_e32 v176, 31, v38
	s_lshl_b32 s92, s79, 5
	v_lshlrev_b32_e32 v32, 2, v0
	s_add_i32 s74, s92, s74
	v_sub_u32_e32 v1, v176, v32
	v_lshlrev_b32_e32 v175, 4, v0
	s_lshl_b32 s2, s79, 3
	v_bfe_u32 v0, v38, 4, 2
	v_add_u32_e32 v179, s74, v1
	v_or_b32_e32 v1, s2, v0
	v_and_b32_e32 v2, 15, v38
	v_and_b32_e32 v39, 63, v38
	v_bitop3_b32 v3, v0, v38, 15 bitop3:0x78
	v_mul_lo_u32 v1, v1, s14
	v_bitop3_b32 v0, v0, v2, 4 bitop3:0x36
	s_mul_i32 s4, s79, 0x1c00
	s_waitcnt vmcnt(16)
	v_lshlrev_b32_e32 v40, 4, v39
	v_lshl_or_b32 v0, v0, 4, v1
	s_lshl_b32 s78, s79, 11
	v_readlane_b32 s7, v255, 53
	s_lshl_b32 s3, s79, 12
	s_add_i32 s4, s5, s4
	v_lshl_or_b32 v160, v3, 4, v1
	v_add_u32_e32 v170, 0x1a000, v0
	s_add_i32 s78, s78, s7
	s_add_i32 s98, s79, 2
	s_lshr_b32 s98, s98, 2
	s_lshl_b32 s98, s98, 7
	s_add_i32 s78, s78, s98
	s_add_i32 s3, s3, s33
	v_add_u32_e32 v180, s4, v40
	s_waitcnt vmcnt(16) lgkmcnt(0)
	ds_write_b128 v180, v[128:131]
	ds_write_b128 v180, v[132:135] offset:1024
	ds_write_b128 v180, v[136:139] offset:2048
	ds_write_b128 v180, v[140:143] offset:3072
	ds_write_b128 v180, v[144:147] offset:4096
	ds_write_b128 v180, v[148:151] offset:5120
	ds_write_b128 v180, v[152:155] offset:6144
	s_add_u32 s4, s66, 0x1a2900
	s_addc_u32 s5, s67, 0
	v_lshl_add_u64 v[0:1], s[4:5], 0, v[160:161]
	s_add_i32 s82, s78, 0x4100
	s_mov_b32 s6, m0
	s_mov_b32 m0, s82
	s_nop 0
	global_load_lds_dwordx4 v[0:1], off
	s_mov_b32 m0, s6
	v_mov_b32_e32 v171, v161
	v_lshl_add_u64 v[0:1], s[4:5], 0, v[170:171]
	s_add_i32 s84, s78, 0x4500
	s_mov_b32 s4, m0
	s_mov_b32 m0, s84
	s_nop 0
	global_load_lds_dwordx4 v[0:1], off
	s_mov_b32 m0, s4
	s_waitcnt lgkmcnt(0)
	s_barrier
	v_lshlrev_b32_e32 v0, 4, v38
	s_movk_i32 s4, 0x70
	v_and_b32_e32 v33, 16, v176
	v_lshlrev_b32_e32 v33, 3, v33
	v_lshl_add_u32 v33, v176, 8, v33
	v_and_b32_e32 v1, 0x70, v0
	v_bitop3_b32 v34, v175, v0, s4 bitop3:0x78
	s_movk_i32 s4, 0x60
	v_add_u32_e32 v2, s7, v33
	v_bitop3_b32 v35, v175, v1, 32 bitop3:0x36
	v_bitop3_b32 v36, v175, v1, 64 bitop3:0x36
	v_bitop3_b32 v37, v175, v1, s4 bitop3:0x36
	v_add_u32_e32 v181, v34, v2
	v_add_u32_e32 v182, v35, v2
	v_add_u32_e32 v183, v36, v2
	v_add_u32_e32 v184, v37, v2
	ds_read_b128 v[0:3], v181 offset:0
	ds_read_b128 v[4:7], v181 offset:0x2080
	ds_read_b128 v[8:11], v180 offset:0
	ds_read_b128 v[42:45], v182 offset:0
	ds_read_b128 v[46:49], v182 offset:0x2080
	ds_read_b128 v[50:53], v180 offset:0x400
	s_waitcnt lgkmcnt(3)
	s_nop 0
	v_mfma_f32_32x32x16_bf16 v[16:31], v[0:3], v[8:11], 0
	v_mfma_f32_32x32x16_bf16 v[0:15], v[4:7], v[8:11], 0
	ds_read_b128 v[54:57], v183 offset:0
	ds_read_b128 v[58:61], v183 offset:0x2080
	ds_read_b128 v[62:65], v180 offset:0x800
	s_waitcnt lgkmcnt(3)
	v_mfma_f32_32x32x16_bf16 v[16:31], v[42:45], v[50:53], v[16:31]
	v_mfma_f32_32x32x16_bf16 v[0:15], v[46:49], v[50:53], v[0:15]
	ds_read_b128 v[42:45], v184 offset:0
	ds_read_b128 v[46:49], v184 offset:0x2080
	ds_read_b128 v[50:53], v180 offset:0xc00
	s_waitcnt lgkmcnt(3)
	v_mfma_f32_32x32x16_bf16 v[16:31], v[54:57], v[62:65], v[16:31]
	v_mfma_f32_32x32x16_bf16 v[0:15], v[58:61], v[62:65], v[0:15]
	ds_read_b128 v[54:57], v181 offset:0x80
	ds_read_b128 v[58:61], v181 offset:0x2100
	ds_read_b128 v[62:65], v180 offset:0x1000
	s_waitcnt lgkmcnt(3)
	v_mfma_f32_32x32x16_bf16 v[16:31], v[42:45], v[50:53], v[16:31]
	v_mfma_f32_32x32x16_bf16 v[0:15], v[46:49], v[50:53], v[0:15]
	ds_read_b128 v[42:45], v182 offset:0x80
	ds_read_b128 v[46:49], v182 offset:0x2100
	ds_read_b128 v[50:53], v180 offset:0x1400
	s_waitcnt lgkmcnt(3)
	v_mfma_f32_32x32x16_bf16 v[16:31], v[54:57], v[62:65], v[16:31]
	v_mfma_f32_32x32x16_bf16 v[0:15], v[58:61], v[62:65], v[0:15]
	ds_read_b128 v[54:57], v183 offset:0x80
	ds_read_b128 v[58:61], v183 offset:0x2100
	ds_read_b128 v[62:65], v180 offset:0x1800
	s_waitcnt lgkmcnt(3)
	v_mfma_f32_32x32x16_bf16 v[16:31], v[42:45], v[50:53], v[16:31]
	v_mfma_f32_32x32x16_bf16 v[0:15], v[46:49], v[50:53], v[0:15]
	ds_read_b128 v[42:45], v184 offset:0x80
	ds_read_b128 v[46:49], v184 offset:0x2100
	s_waitcnt lgkmcnt(2)
	v_mfma_f32_32x32x16_bf16 v[16:31], v[54:57], v[62:65], v[16:31]
	v_mfma_f32_32x32x16_bf16 v[0:15], v[58:61], v[62:65], v[0:15]
	s_waitcnt lgkmcnt(0)
	v_mfma_f32_32x32x16_bf16 v[16:31], v[42:45], v[166:169], v[16:31]
	v_mfma_f32_32x32x16_bf16 v[0:15], v[46:49], v[166:169], v[0:15]
	s_bitcmp0_b32 s100, 8
	s_cbranch_scc1 .Lstg_a17
	s_waitcnt vmcnt(0)
	s_waitcnt lgkmcnt(0)
	s_barrier

.LBB0_589:
	ds_read_b64_tr_b16 v[144:145], v177 offset:0
	ds_read_b64_tr_b16 v[146:147], v177 offset:0x1000
	ds_read_b64_tr_b16 v[148:149], v177 offset:0x2000
	ds_read_b64_tr_b16 v[150:151], v177 offset:0x3000
	ds_read_b64_tr_b16 v[152:153], v177 offset:0x4000
	ds_read_b64_tr_b16 v[154:155], v177 offset:0x5000
	ds_read_b64_tr_b16 v[156:157], v177 offset:0x6000
	ds_read_b64_tr_b16 v[158:159], v177 offset:0x7000
	ds_read_b64_tr_b16 v[192:193], v177 offset:0x200
	ds_read_b64_tr_b16 v[194:195], v177 offset:0x1200
	ds_read_b64_tr_b16 v[196:197], v177 offset:0x2200
	ds_read_b64_tr_b16 v[198:199], v177 offset:0x3200
	ds_read_b64_tr_b16 v[200:201], v177 offset:0x4200
	ds_read_b64_tr_b16 v[202:203], v177 offset:0x5200
	ds_read_b64_tr_b16 v[204:205], v177 offset:0x6200
	ds_read_b64_tr_b16 v[206:207], v177 offset:0x7200
	s_waitcnt lgkmcnt(8)
	s_nop 0
	v_mfma_f32_32x32x16_bf16 v[112:127], v[144:147], v[128:131], v[112:127]
	v_mfma_f32_32x32x16_bf16 v[112:127], v[148:151], v[132:135], v[112:127]
	v_mfma_f32_32x32x16_bf16 v[112:127], v[152:155], v[136:139], v[112:127]
	v_mfma_f32_32x32x16_bf16 v[112:127], v[156:159], v[140:143], v[112:127]
	ds_read_b64_tr_b16 v[144:145], v177 offset:0x400
	ds_read_b64_tr_b16 v[146:147], v177 offset:0x1400
	ds_read_b64_tr_b16 v[148:149], v177 offset:0x2400
	ds_read_b64_tr_b16 v[150:151], v177 offset:0x3400
	ds_read_b64_tr_b16 v[152:153], v177 offset:0x4400
	ds_read_b64_tr_b16 v[154:155], v177 offset:0x5400
	ds_read_b64_tr_b16 v[156:157], v177 offset:0x6400
	ds_read_b64_tr_b16 v[158:159], v177 offset:0x7400
	s_waitcnt lgkmcnt(8)
	v_mfma_f32_32x32x16_bf16 v[96:111], v[192:195], v[128:131], v[96:111]
	v_mfma_f32_32x32x16_bf16 v[96:111], v[196:199], v[132:135], v[96:111]
	v_mfma_f32_32x32x16_bf16 v[96:111], v[200:203], v[136:139], v[96:111]
	v_mfma_f32_32x32x16_bf16 v[96:111], v[204:207], v[140:143], v[96:111]
	ds_read_b64_tr_b16 v[192:193], v177 offset:0x600
	ds_read_b64_tr_b16 v[194:195], v177 offset:0x1600
	ds_read_b64_tr_b16 v[196:197], v177 offset:0x2600
	ds_read_b64_tr_b16 v[198:199], v177 offset:0x3600
	ds_read_b64_tr_b16 v[200:201], v177 offset:0x4600
	ds_read_b64_tr_b16 v[202:203], v177 offset:0x5600
	ds_read_b64_tr_b16 v[204:205], v177 offset:0x6600
	ds_read_b64_tr_b16 v[206:207], v177 offset:0x7600
	s_waitcnt lgkmcnt(8)
	v_mfma_f32_32x32x16_bf16 v[80:95], v[144:147], v[128:131], v[80:95]
	v_mfma_f32_32x32x16_bf16 v[80:95], v[148:151], v[132:135], v[80:95]
	v_mfma_f32_32x32x16_bf16 v[80:95], v[152:155], v[136:139], v[80:95]
	v_mfma_f32_32x32x16_bf16 v[80:95], v[156:159], v[140:143], v[80:95]
	ds_read_b64_tr_b16 v[144:145], v177 offset:0x800
	ds_read_b64_tr_b16 v[146:147], v177 offset:0x1800
	ds_read_b64_tr_b16 v[148:149], v177 offset:0x2800
	ds_read_b64_tr_b16 v[150:151], v177 offset:0x3800
	ds_read_b64_tr_b16 v[152:153], v177 offset:0x4800
	ds_read_b64_tr_b16 v[154:155], v177 offset:0x5800
	ds_read_b64_tr_b16 v[156:157], v177 offset:0x6800
	ds_read_b64_tr_b16 v[158:159], v177 offset:0x7800
	s_waitcnt lgkmcnt(8)
	v_mfma_f32_32x32x16_bf16 v[64:79], v[192:195], v[128:131], v[64:79]
	v_mfma_f32_32x32x16_bf16 v[64:79], v[196:199], v[132:135], v[64:79]
	v_mfma_f32_32x32x16_bf16 v[64:79], v[200:203], v[136:139], v[64:79]
	v_mfma_f32_32x32x16_bf16 v[64:79], v[204:207], v[140:143], v[64:79]
	ds_read_b64_tr_b16 v[192:193], v177 offset:0xa00
	ds_read_b64_tr_b16 v[194:195], v177 offset:0x1a00
	ds_read_b64_tr_b16 v[196:197], v177 offset:0x2a00
	ds_read_b64_tr_b16 v[198:199], v177 offset:0x3a00
	ds_read_b64_tr_b16 v[200:201], v177 offset:0x4a00
	ds_read_b64_tr_b16 v[202:203], v177 offset:0x5a00
	ds_read_b64_tr_b16 v[204:205], v177 offset:0x6a00
	ds_read_b64_tr_b16 v[206:207], v177 offset:0x7a00
	s_waitcnt lgkmcnt(8)
	v_mfma_f32_32x32x16_bf16 v[48:63], v[144:147], v[128:131], v[48:63]
	v_mfma_f32_32x32x16_bf16 v[48:63], v[148:151], v[132:135], v[48:63]
	v_mfma_f32_32x32x16_bf16 v[48:63], v[152:155], v[136:139], v[48:63]
	v_mfma_f32_32x32x16_bf16 v[48:63], v[156:159], v[140:143], v[48:63]
	ds_read_b64_tr_b16 v[144:145], v177 offset:0xc00
	ds_read_b64_tr_b16 v[146:147], v177 offset:0x1c00
	ds_read_b64_tr_b16 v[148:149], v177 offset:0x2c00
	ds_read_b64_tr_b16 v[150:151], v177 offset:0x3c00
	ds_read_b64_tr_b16 v[152:153], v177 offset:0x4c00
	ds_read_b64_tr_b16 v[154:155], v177 offset:0x5c00
	ds_read_b64_tr_b16 v[156:157], v177 offset:0x6c00
	ds_read_b64_tr_b16 v[158:159], v177 offset:0x7c00
	s_waitcnt lgkmcnt(8)
	v_mfma_f32_32x32x16_bf16 v[32:47], v[192:195], v[128:131], v[32:47]
	v_mfma_f32_32x32x16_bf16 v[32:47], v[196:199], v[132:135], v[32:47]
	v_mfma_f32_32x32x16_bf16 v[32:47], v[200:203], v[136:139], v[32:47]
	v_mfma_f32_32x32x16_bf16 v[32:47], v[204:207], v[140:143], v[32:47]
	ds_read_b64_tr_b16 v[192:193], v177 offset:0xe00
	ds_read_b64_tr_b16 v[194:195], v177 offset:0x1e00
	ds_read_b64_tr_b16 v[196:197], v177 offset:0x2e00
	ds_read_b64_tr_b16 v[198:199], v177 offset:0x3e00
	ds_read_b64_tr_b16 v[200:201], v177 offset:0x4e00
	ds_read_b64_tr_b16 v[202:203], v177 offset:0x5e00
	ds_read_b64_tr_b16 v[204:205], v177 offset:0x6e00
	ds_read_b64_tr_b16 v[206:207], v177 offset:0x7e00
	s_waitcnt lgkmcnt(8)
	v_mfma_f32_32x32x16_bf16 v[16:31], v[144:147], v[128:131], v[16:31]
	v_mfma_f32_32x32x16_bf16 v[16:31], v[148:151], v[132:135], v[16:31]
	v_mfma_f32_32x32x16_bf16 v[16:31], v[152:155], v[136:139], v[16:31]
	v_mfma_f32_32x32x16_bf16 v[16:31], v[156:159], v[140:143], v[16:31]
	s_waitcnt lgkmcnt(0)
	v_mfma_f32_32x32x16_bf16 v[0:15], v[192:195], v[128:131], v[0:15]
	v_mfma_f32_32x32x16_bf16 v[0:15], v[196:199], v[132:135], v[0:15]
	v_mfma_f32_32x32x16_bf16 v[0:15], v[200:203], v[136:139], v[0:15]
	v_mfma_f32_32x32x16_bf16 v[0:15], v[204:207], v[140:143], v[0:15]
	ds_read_b128 v[128:131], v188 offset:0
	ds_read_b128 v[132:135], v188 offset:0x2080
	ds_read_b128 v[136:139], v180 offset:0
	ds_read_b128 v[192:195], v187 offset:0
	ds_read_b128 v[196:199], v187 offset:0x2080
	ds_read_b128 v[200:203], v180 offset:0x400
	s_waitcnt lgkmcnt(3)
	s_nop 0
	v_mfma_f32_32x32x16_bf16 v[144:159], v[128:131], v[136:139], 0
	v_mfma_f32_32x32x16_bf16 v[128:143], v[132:135], v[136:139], 0
	ds_read_b128 v[204:207], v186 offset:0
	ds_read_b128 v[208:211], v186 offset:0x2080
	ds_read_b128 v[212:215], v180 offset:0x800
	s_waitcnt lgkmcnt(3)
	v_mfma_f32_32x32x16_bf16 v[144:159], v[192:195], v[200:203], v[144:159]
	v_mfma_f32_32x32x16_bf16 v[128:143], v[196:199], v[200:203], v[128:143]
	ds_read_b128 v[192:195], v185 offset:0
	ds_read_b128 v[196:199], v185 offset:0x2080
	ds_read_b128 v[200:203], v180 offset:0xc00
	s_waitcnt lgkmcnt(3)
	v_mfma_f32_32x32x16_bf16 v[144:159], v[204:207], v[212:215], v[144:159]
	v_mfma_f32_32x32x16_bf16 v[128:143], v[208:211], v[212:215], v[128:143]
	ds_read_b128 v[204:207], v188 offset:0x80
	ds_read_b128 v[208:211], v188 offset:0x2100
	ds_read_b128 v[212:215], v180 offset:0x1000
	s_waitcnt lgkmcnt(3)
	v_mfma_f32_32x32x16_bf16 v[144:159], v[192:195], v[200:203], v[144:159]
	v_mfma_f32_32x32x16_bf16 v[128:143], v[196:199], v[200:203], v[128:143]
	ds_read_b128 v[192:195], v187 offset:0x80
	ds_read_b128 v[196:199], v187 offset:0x2100
	ds_read_b128 v[200:203], v180 offset:0x1400
	s_waitcnt lgkmcnt(3)
	v_mfma_f32_32x32x16_bf16 v[144:159], v[204:207], v[212:215], v[144:159]
	v_mfma_f32_32x32x16_bf16 v[128:143], v[208:211], v[212:215], v[128:143]
	ds_read_b128 v[204:207], v186 offset:0x80
	ds_read_b128 v[208:211], v186 offset:0x2100
	ds_read_b128 v[212:215], v180 offset:0x1800
	s_waitcnt lgkmcnt(3)
	v_mfma_f32_32x32x16_bf16 v[144:159], v[192:195], v[200:203], v[144:159]
	v_mfma_f32_32x32x16_bf16 v[128:143], v[196:199], v[200:203], v[128:143]
	ds_read_b128 v[192:195], v185 offset:0x80
	ds_read_b128 v[196:199], v185 offset:0x2100
	s_waitcnt lgkmcnt(2)
	v_mfma_f32_32x32x16_bf16 v[144:159], v[204:207], v[212:215], v[144:159]
	v_mfma_f32_32x32x16_bf16 v[128:143], v[208:211], v[212:215], v[128:143]
	s_waitcnt lgkmcnt(0)
	v_mfma_f32_32x32x16_bf16 v[144:159], v[192:195], v[166:169], v[144:159]
	v_mfma_f32_32x32x16_bf16 v[128:143], v[196:199], v[166:169], v[128:143]
	s_bitcmp0_b32 s100, 8
	s_cbranch_scc1 .Lstg_a18
	s_waitcnt vmcnt(0)
	s_waitcnt lgkmcnt(0)
	s_barrier

.LBB0_597:
	ds_read_b64_tr_b16 v[144:145], v177 offset:0x8000
	ds_read_b64_tr_b16 v[146:147], v177 offset:0x9000
	ds_read_b64_tr_b16 v[148:149], v177 offset:0xa000
	ds_read_b64_tr_b16 v[150:151], v177 offset:0xb000
	ds_read_b64_tr_b16 v[152:153], v177 offset:0xc000
	ds_read_b64_tr_b16 v[154:155], v177 offset:0xd000
	ds_read_b64_tr_b16 v[156:157], v177 offset:0xe000
	ds_read_b64_tr_b16 v[158:159], v177 offset:0xf000
	ds_read_b64_tr_b16 v[194:195], v177 offset:0x8200
	ds_read_b64_tr_b16 v[196:197], v177 offset:0x9200
	ds_read_b64_tr_b16 v[198:199], v177 offset:0xa200
	ds_read_b64_tr_b16 v[200:201], v177 offset:0xb200
	ds_read_b64_tr_b16 v[202:203], v177 offset:0xc200
	ds_read_b64_tr_b16 v[204:205], v177 offset:0xd200
	ds_read_b64_tr_b16 v[206:207], v177 offset:0xe200
	ds_read_b64_tr_b16 v[208:209], v177 offset:0xf200
	s_waitcnt lgkmcnt(8)
	s_nop 0
	v_mfma_f32_32x32x16_bf16 v[112:127], v[144:147], v[128:131], v[112:127]
	v_mfma_f32_32x32x16_bf16 v[112:127], v[148:151], v[132:135], v[112:127]
	v_mfma_f32_32x32x16_bf16 v[112:127], v[152:155], v[136:139], v[112:127]
	v_mfma_f32_32x32x16_bf16 v[112:127], v[156:159], v[140:143], v[112:127]
	ds_read_b64_tr_b16 v[144:145], v177 offset:0x8400
	ds_read_b64_tr_b16 v[146:147], v177 offset:0x9400
	ds_read_b64_tr_b16 v[148:149], v177 offset:0xa400
	ds_read_b64_tr_b16 v[150:151], v177 offset:0xb400
	ds_read_b64_tr_b16 v[152:153], v177 offset:0xc400
	ds_read_b64_tr_b16 v[154:155], v177 offset:0xd400
	ds_read_b64_tr_b16 v[156:157], v177 offset:0xe400
	ds_read_b64_tr_b16 v[158:159], v177 offset:0xf400
	s_waitcnt lgkmcnt(8)
	v_mfma_f32_32x32x16_bf16 v[96:111], v[194:197], v[128:131], v[96:111]
	v_mfma_f32_32x32x16_bf16 v[96:111], v[198:201], v[132:135], v[96:111]
	v_mfma_f32_32x32x16_bf16 v[96:111], v[202:205], v[136:139], v[96:111]
	v_mfma_f32_32x32x16_bf16 v[96:111], v[206:209], v[140:143], v[96:111]
	ds_read_b64_tr_b16 v[194:195], v177 offset:0x8600
	ds_read_b64_tr_b16 v[196:197], v177 offset:0x9600
	ds_read_b64_tr_b16 v[198:199], v177 offset:0xa600
	ds_read_b64_tr_b16 v[200:201], v177 offset:0xb600
	ds_read_b64_tr_b16 v[202:203], v177 offset:0xc600
	ds_read_b64_tr_b16 v[204:205], v177 offset:0xd600
	ds_read_b64_tr_b16 v[206:207], v177 offset:0xe600
	ds_read_b64_tr_b16 v[208:209], v177 offset:0xf600
	s_waitcnt lgkmcnt(8)
	v_mfma_f32_32x32x16_bf16 v[80:95], v[144:147], v[128:131], v[80:95]
	v_mfma_f32_32x32x16_bf16 v[80:95], v[148:151], v[132:135], v[80:95]
	v_mfma_f32_32x32x16_bf16 v[80:95], v[152:155], v[136:139], v[80:95]
	v_mfma_f32_32x32x16_bf16 v[80:95], v[156:159], v[140:143], v[80:95]
	ds_read_b64_tr_b16 v[144:145], v177 offset:0x8800
	ds_read_b64_tr_b16 v[146:147], v177 offset:0x9800
	ds_read_b64_tr_b16 v[148:149], v177 offset:0xa800
	ds_read_b64_tr_b16 v[150:151], v177 offset:0xb800
	ds_read_b64_tr_b16 v[152:153], v177 offset:0xc800
	ds_read_b64_tr_b16 v[154:155], v177 offset:0xd800
	ds_read_b64_tr_b16 v[156:157], v177 offset:0xe800
	ds_read_b64_tr_b16 v[158:159], v177 offset:0xf800
	s_waitcnt lgkmcnt(8)
	v_mfma_f32_32x32x16_bf16 v[64:79], v[194:197], v[128:131], v[64:79]
	v_mfma_f32_32x32x16_bf16 v[64:79], v[198:201], v[132:135], v[64:79]
	v_mfma_f32_32x32x16_bf16 v[64:79], v[202:205], v[136:139], v[64:79]
	v_mfma_f32_32x32x16_bf16 v[64:79], v[206:209], v[140:143], v[64:79]
	ds_read_b64_tr_b16 v[194:195], v177 offset:0x8a00
	ds_read_b64_tr_b16 v[196:197], v177 offset:0x9a00
	ds_read_b64_tr_b16 v[198:199], v177 offset:0xaa00
	ds_read_b64_tr_b16 v[200:201], v177 offset:0xba00
	ds_read_b64_tr_b16 v[202:203], v177 offset:0xca00
	ds_read_b64_tr_b16 v[204:205], v177 offset:0xda00
	ds_read_b64_tr_b16 v[206:207], v177 offset:0xea00
	ds_read_b64_tr_b16 v[208:209], v177 offset:0xfa00
	s_waitcnt lgkmcnt(8)
	v_mfma_f32_32x32x16_bf16 v[48:63], v[144:147], v[128:131], v[48:63]
	v_mfma_f32_32x32x16_bf16 v[48:63], v[148:151], v[132:135], v[48:63]
	v_mfma_f32_32x32x16_bf16 v[48:63], v[152:155], v[136:139], v[48:63]
	v_mfma_f32_32x32x16_bf16 v[48:63], v[156:159], v[140:143], v[48:63]
	ds_read_b64_tr_b16 v[144:145], v177 offset:0x8c00
	ds_read_b64_tr_b16 v[146:147], v177 offset:0x9c00
	ds_read_b64_tr_b16 v[148:149], v177 offset:0xac00
	ds_read_b64_tr_b16 v[150:151], v177 offset:0xbc00
	ds_read_b64_tr_b16 v[152:153], v177 offset:0xcc00
	ds_read_b64_tr_b16 v[154:155], v177 offset:0xdc00
	ds_read_b64_tr_b16 v[156:157], v177 offset:0xec00
	ds_read_b64_tr_b16 v[158:159], v177 offset:0xfc00
	s_waitcnt lgkmcnt(8)
	v_mfma_f32_32x32x16_bf16 v[32:47], v[194:197], v[128:131], v[32:47]
	v_mfma_f32_32x32x16_bf16 v[32:47], v[198:201], v[132:135], v[32:47]
	v_mfma_f32_32x32x16_bf16 v[32:47], v[202:205], v[136:139], v[32:47]
	v_mfma_f32_32x32x16_bf16 v[32:47], v[206:209], v[140:143], v[32:47]
	ds_read_b64_tr_b16 v[194:195], v177 offset:0x8e00
	ds_read_b64_tr_b16 v[196:197], v177 offset:0x9e00
	ds_read_b64_tr_b16 v[198:199], v177 offset:0xae00
	ds_read_b64_tr_b16 v[200:201], v177 offset:0xbe00
	ds_read_b64_tr_b16 v[202:203], v177 offset:0xce00
	ds_read_b64_tr_b16 v[204:205], v177 offset:0xde00
	ds_read_b64_tr_b16 v[206:207], v177 offset:0xee00
	ds_read_b64_tr_b16 v[208:209], v177 offset:0xfe00
	s_waitcnt lgkmcnt(8)
	v_mfma_f32_32x32x16_bf16 v[16:31], v[144:147], v[128:131], v[16:31]
	v_mfma_f32_32x32x16_bf16 v[16:31], v[148:151], v[132:135], v[16:31]
	v_mfma_f32_32x32x16_bf16 v[16:31], v[152:155], v[136:139], v[16:31]
	v_mfma_f32_32x32x16_bf16 v[16:31], v[156:159], v[140:143], v[16:31]
	s_waitcnt lgkmcnt(0)
	v_mfma_f32_32x32x16_bf16 v[0:15], v[194:197], v[128:131], v[0:15]
	v_mfma_f32_32x32x16_bf16 v[0:15], v[198:201], v[132:135], v[0:15]
	v_mfma_f32_32x32x16_bf16 v[0:15], v[202:205], v[136:139], v[0:15]
	v_mfma_f32_32x32x16_bf16 v[0:15], v[206:209], v[140:143], v[0:15]
	ds_read_b128 v[128:131], v181 offset:0
	ds_read_b128 v[132:135], v181 offset:0x2080
	ds_read_b128 v[136:139], v180 offset:0
	ds_read_b128 v[194:197], v182 offset:0
	ds_read_b128 v[198:201], v182 offset:0x2080
	ds_read_b128 v[202:205], v180 offset:0x400
	s_waitcnt lgkmcnt(3)
	s_nop 0
	v_mfma_f32_32x32x16_bf16 v[144:159], v[128:131], v[136:139], 0
	v_mfma_f32_32x32x16_bf16 v[128:143], v[132:135], v[136:139], 0
	ds_read_b128 v[206:209], v183 offset:0
	ds_read_b128 v[210:213], v183 offset:0x2080
	ds_read_b128 v[214:217], v180 offset:0x800
	s_waitcnt lgkmcnt(3)
	v_mfma_f32_32x32x16_bf16 v[144:159], v[194:197], v[202:205], v[144:159]
	v_mfma_f32_32x32x16_bf16 v[128:143], v[198:201], v[202:205], v[128:143]
	ds_read_b128 v[194:197], v184 offset:0
	ds_read_b128 v[198:201], v184 offset:0x2080
	ds_read_b128 v[202:205], v180 offset:0xc00
	s_waitcnt lgkmcnt(3)
	v_mfma_f32_32x32x16_bf16 v[144:159], v[206:209], v[214:217], v[144:159]
	v_mfma_f32_32x32x16_bf16 v[128:143], v[210:213], v[214:217], v[128:143]
	ds_read_b128 v[206:209], v181 offset:0x80
	ds_read_b128 v[210:213], v181 offset:0x2100
	ds_read_b128 v[214:217], v180 offset:0x1000
	s_waitcnt lgkmcnt(3)
	v_mfma_f32_32x32x16_bf16 v[144:159], v[194:197], v[202:205], v[144:159]
	v_mfma_f32_32x32x16_bf16 v[128:143], v[198:201], v[202:205], v[128:143]
	ds_read_b128 v[194:197], v182 offset:0x80
	ds_read_b128 v[198:201], v182 offset:0x2100
	ds_read_b128 v[202:205], v180 offset:0x1400
	s_waitcnt lgkmcnt(3)
	v_mfma_f32_32x32x16_bf16 v[144:159], v[206:209], v[214:217], v[144:159]
	v_mfma_f32_32x32x16_bf16 v[128:143], v[210:213], v[214:217], v[128:143]
	ds_read_b128 v[206:209], v183 offset:0x80
	ds_read_b128 v[210:213], v183 offset:0x2100
	ds_read_b128 v[214:217], v180 offset:0x1800
	s_waitcnt lgkmcnt(3)
	v_mfma_f32_32x32x16_bf16 v[144:159], v[194:197], v[202:205], v[144:159]
	v_mfma_f32_32x32x16_bf16 v[128:143], v[198:201], v[202:205], v[128:143]
	ds_read_b128 v[194:197], v184 offset:0x80
	ds_read_b128 v[198:201], v184 offset:0x2100
	s_waitcnt lgkmcnt(2)
	v_mfma_f32_32x32x16_bf16 v[144:159], v[206:209], v[214:217], v[144:159]
	v_mfma_f32_32x32x16_bf16 v[128:143], v[210:213], v[214:217], v[128:143]
	s_waitcnt lgkmcnt(0)
	v_mfma_f32_32x32x16_bf16 v[144:159], v[194:197], v[166:169], v[144:159]
	v_mfma_f32_32x32x16_bf16 v[128:143], v[198:201], v[166:169], v[128:143]
	s_bitcmp0_b32 s100, 8
	s_cbranch_scc1 .Lstg_a19
	s_waitcnt vmcnt(0)
	s_waitcnt lgkmcnt(0)
	s_barrier

.LBB0_612:
	ds_read_b64_tr_b16 v[144:145], v177 offset:0
	ds_read_b64_tr_b16 v[146:147], v177 offset:0x1000
	ds_read_b64_tr_b16 v[148:149], v177 offset:0x2000
	ds_read_b64_tr_b16 v[150:151], v177 offset:0x3000
	ds_read_b64_tr_b16 v[152:153], v177 offset:0x4000
	ds_read_b64_tr_b16 v[154:155], v177 offset:0x5000
	ds_read_b64_tr_b16 v[156:157], v177 offset:0x6000
	ds_read_b64_tr_b16 v[158:159], v177 offset:0x7000
	ds_read_b64_tr_b16 v[192:193], v177 offset:0x200
	ds_read_b64_tr_b16 v[194:195], v177 offset:0x1200
	ds_read_b64_tr_b16 v[196:197], v177 offset:0x2200
	ds_read_b64_tr_b16 v[198:199], v177 offset:0x3200
	ds_read_b64_tr_b16 v[200:201], v177 offset:0x4200
	ds_read_b64_tr_b16 v[202:203], v177 offset:0x5200
	ds_read_b64_tr_b16 v[204:205], v177 offset:0x6200
	ds_read_b64_tr_b16 v[206:207], v177 offset:0x7200
	s_waitcnt lgkmcnt(8)
	s_nop 0
	v_mfma_f32_32x32x16_bf16 v[112:127], v[144:147], v[128:131], v[112:127]
	v_mfma_f32_32x32x16_bf16 v[112:127], v[148:151], v[132:135], v[112:127]
	v_mfma_f32_32x32x16_bf16 v[112:127], v[152:155], v[136:139], v[112:127]
	v_mfma_f32_32x32x16_bf16 v[112:127], v[156:159], v[140:143], v[112:127]
	ds_read_b64_tr_b16 v[144:145], v177 offset:0x400
	ds_read_b64_tr_b16 v[146:147], v177 offset:0x1400
	ds_read_b64_tr_b16 v[148:149], v177 offset:0x2400
	ds_read_b64_tr_b16 v[150:151], v177 offset:0x3400
	ds_read_b64_tr_b16 v[152:153], v177 offset:0x4400
	ds_read_b64_tr_b16 v[154:155], v177 offset:0x5400
	ds_read_b64_tr_b16 v[156:157], v177 offset:0x6400
	ds_read_b64_tr_b16 v[158:159], v177 offset:0x7400
	s_waitcnt lgkmcnt(8)
	v_mfma_f32_32x32x16_bf16 v[96:111], v[192:195], v[128:131], v[96:111]
	v_mfma_f32_32x32x16_bf16 v[96:111], v[196:199], v[132:135], v[96:111]
	v_mfma_f32_32x32x16_bf16 v[96:111], v[200:203], v[136:139], v[96:111]
	v_mfma_f32_32x32x16_bf16 v[96:111], v[204:207], v[140:143], v[96:111]
	ds_read_b64_tr_b16 v[192:193], v177 offset:0x600
	ds_read_b64_tr_b16 v[194:195], v177 offset:0x1600
	ds_read_b64_tr_b16 v[196:197], v177 offset:0x2600
	ds_read_b64_tr_b16 v[198:199], v177 offset:0x3600
	ds_read_b64_tr_b16 v[200:201], v177 offset:0x4600
	ds_read_b64_tr_b16 v[202:203], v177 offset:0x5600
	ds_read_b64_tr_b16 v[204:205], v177 offset:0x6600
	ds_read_b64_tr_b16 v[206:207], v177 offset:0x7600
	s_waitcnt lgkmcnt(8)
	v_mfma_f32_32x32x16_bf16 v[80:95], v[144:147], v[128:131], v[80:95]
	v_mfma_f32_32x32x16_bf16 v[80:95], v[148:151], v[132:135], v[80:95]
	v_mfma_f32_32x32x16_bf16 v[80:95], v[152:155], v[136:139], v[80:95]
	v_mfma_f32_32x32x16_bf16 v[80:95], v[156:159], v[140:143], v[80:95]
	ds_read_b64_tr_b16 v[144:145], v177 offset:0x800
	ds_read_b64_tr_b16 v[146:147], v177 offset:0x1800
	ds_read_b64_tr_b16 v[148:149], v177 offset:0x2800
	ds_read_b64_tr_b16 v[150:151], v177 offset:0x3800
	ds_read_b64_tr_b16 v[152:153], v177 offset:0x4800
	ds_read_b64_tr_b16 v[154:155], v177 offset:0x5800
	ds_read_b64_tr_b16 v[156:157], v177 offset:0x6800
	ds_read_b64_tr_b16 v[158:159], v177 offset:0x7800
	s_waitcnt lgkmcnt(8)
	v_mfma_f32_32x32x16_bf16 v[64:79], v[192:195], v[128:131], v[64:79]
	v_mfma_f32_32x32x16_bf16 v[64:79], v[196:199], v[132:135], v[64:79]
	v_mfma_f32_32x32x16_bf16 v[64:79], v[200:203], v[136:139], v[64:79]
	v_mfma_f32_32x32x16_bf16 v[64:79], v[204:207], v[140:143], v[64:79]
	ds_read_b64_tr_b16 v[192:193], v177 offset:0xa00
	ds_read_b64_tr_b16 v[194:195], v177 offset:0x1a00
	ds_read_b64_tr_b16 v[196:197], v177 offset:0x2a00
	ds_read_b64_tr_b16 v[198:199], v177 offset:0x3a00
	ds_read_b64_tr_b16 v[200:201], v177 offset:0x4a00
	ds_read_b64_tr_b16 v[202:203], v177 offset:0x5a00
	ds_read_b64_tr_b16 v[204:205], v177 offset:0x6a00
	ds_read_b64_tr_b16 v[206:207], v177 offset:0x7a00
	s_waitcnt lgkmcnt(8)
	v_mfma_f32_32x32x16_bf16 v[48:63], v[144:147], v[128:131], v[48:63]
	v_mfma_f32_32x32x16_bf16 v[48:63], v[148:151], v[132:135], v[48:63]
	v_mfma_f32_32x32x16_bf16 v[48:63], v[152:155], v[136:139], v[48:63]
	v_mfma_f32_32x32x16_bf16 v[48:63], v[156:159], v[140:143], v[48:63]
	ds_read_b64_tr_b16 v[144:145], v177 offset:0xc00
	ds_read_b64_tr_b16 v[146:147], v177 offset:0x1c00
	ds_read_b64_tr_b16 v[148:149], v177 offset:0x2c00
	ds_read_b64_tr_b16 v[150:151], v177 offset:0x3c00
	ds_read_b64_tr_b16 v[152:153], v177 offset:0x4c00
	ds_read_b64_tr_b16 v[154:155], v177 offset:0x5c00
	ds_read_b64_tr_b16 v[156:157], v177 offset:0x6c00
	ds_read_b64_tr_b16 v[158:159], v177 offset:0x7c00
	s_waitcnt lgkmcnt(8)
	v_mfma_f32_32x32x16_bf16 v[32:47], v[192:195], v[128:131], v[32:47]
	v_mfma_f32_32x32x16_bf16 v[32:47], v[196:199], v[132:135], v[32:47]
	v_mfma_f32_32x32x16_bf16 v[32:47], v[200:203], v[136:139], v[32:47]
	v_mfma_f32_32x32x16_bf16 v[32:47], v[204:207], v[140:143], v[32:47]
	ds_read_b64_tr_b16 v[192:193], v177 offset:0xe00
	ds_read_b64_tr_b16 v[194:195], v177 offset:0x1e00
	ds_read_b64_tr_b16 v[196:197], v177 offset:0x2e00
	ds_read_b64_tr_b16 v[198:199], v177 offset:0x3e00
	ds_read_b64_tr_b16 v[200:201], v177 offset:0x4e00
	ds_read_b64_tr_b16 v[202:203], v177 offset:0x5e00
	ds_read_b64_tr_b16 v[204:205], v177 offset:0x6e00
	ds_read_b64_tr_b16 v[206:207], v177 offset:0x7e00
	s_waitcnt lgkmcnt(8)
	v_mfma_f32_32x32x16_bf16 v[16:31], v[144:147], v[128:131], v[16:31]
	v_mfma_f32_32x32x16_bf16 v[16:31], v[148:151], v[132:135], v[16:31]
	v_mfma_f32_32x32x16_bf16 v[16:31], v[152:155], v[136:139], v[16:31]
	v_mfma_f32_32x32x16_bf16 v[16:31], v[156:159], v[140:143], v[16:31]
	s_waitcnt lgkmcnt(0)
	v_mfma_f32_32x32x16_bf16 v[0:15], v[192:195], v[128:131], v[0:15]
	v_mfma_f32_32x32x16_bf16 v[0:15], v[196:199], v[132:135], v[0:15]
	v_mfma_f32_32x32x16_bf16 v[0:15], v[200:203], v[136:139], v[0:15]
	v_mfma_f32_32x32x16_bf16 v[0:15], v[204:207], v[140:143], v[0:15]
	ds_read_b128 v[128:131], v188 offset:0
	ds_read_b128 v[132:135], v188 offset:0x2080
	ds_read_b128 v[136:139], v180 offset:0
	ds_read_b128 v[192:195], v187 offset:0
	ds_read_b128 v[196:199], v187 offset:0x2080
	ds_read_b128 v[200:203], v180 offset:0x400
	s_waitcnt lgkmcnt(3)
	s_nop 0
	v_mfma_f32_32x32x16_bf16 v[144:159], v[128:131], v[136:139], 0
	v_mfma_f32_32x32x16_bf16 v[128:143], v[132:135], v[136:139], 0
	ds_read_b128 v[204:207], v186 offset:0
	ds_read_b128 v[208:211], v186 offset:0x2080
	ds_read_b128 v[212:215], v180 offset:0x800
	s_waitcnt lgkmcnt(3)
	v_mfma_f32_32x32x16_bf16 v[144:159], v[192:195], v[200:203], v[144:159]
	v_mfma_f32_32x32x16_bf16 v[128:143], v[196:199], v[200:203], v[128:143]
	ds_read_b128 v[192:195], v185 offset:0
	ds_read_b128 v[196:199], v185 offset:0x2080
	ds_read_b128 v[200:203], v180 offset:0xc00
	s_waitcnt lgkmcnt(3)
	v_mfma_f32_32x32x16_bf16 v[144:159], v[204:207], v[212:215], v[144:159]
	v_mfma_f32_32x32x16_bf16 v[128:143], v[208:211], v[212:215], v[128:143]
	ds_read_b128 v[204:207], v188 offset:0x80
	ds_read_b128 v[208:211], v188 offset:0x2100
	ds_read_b128 v[212:215], v180 offset:0x1000
	s_waitcnt lgkmcnt(3)
	v_mfma_f32_32x32x16_bf16 v[144:159], v[192:195], v[200:203], v[144:159]
	v_mfma_f32_32x32x16_bf16 v[128:143], v[196:199], v[200:203], v[128:143]
	ds_read_b128 v[192:195], v187 offset:0x80
	ds_read_b128 v[196:199], v187 offset:0x2100
	ds_read_b128 v[200:203], v180 offset:0x1400
	s_waitcnt lgkmcnt(3)
	v_mfma_f32_32x32x16_bf16 v[144:159], v[204:207], v[212:215], v[144:159]
	v_mfma_f32_32x32x16_bf16 v[128:143], v[208:211], v[212:215], v[128:143]
	ds_read_b128 v[204:207], v186 offset:0x80
	ds_read_b128 v[208:211], v186 offset:0x2100
	ds_read_b128 v[186:189], v180 offset:0x1800
	s_waitcnt lgkmcnt(3)
	v_mfma_f32_32x32x16_bf16 v[144:159], v[192:195], v[200:203], v[144:159]
	v_mfma_f32_32x32x16_bf16 v[128:143], v[196:199], v[200:203], v[128:143]
	ds_read_b128 v[180:183], v185 offset:0x80
	ds_read_b128 v[192:195], v185 offset:0x2100
	s_waitcnt lgkmcnt(2)
	v_mfma_f32_32x32x16_bf16 v[144:159], v[204:207], v[186:189], v[144:159]
	v_mfma_f32_32x32x16_bf16 v[128:143], v[208:211], v[186:189], v[128:143]
	s_waitcnt lgkmcnt(0)
	v_mfma_f32_32x32x16_bf16 v[144:159], v[180:183], v[166:169], v[144:159]
	v_mfma_f32_32x32x16_bf16 v[128:143], v[192:195], v[166:169], v[128:143]
	s_bitcmp0_b32 s100, 8
	s_cbranch_scc1 .Lstg_a20
	s_waitcnt vmcnt(0)
	s_waitcnt lgkmcnt(0)
	s_barrier
